# in1_slot0_rowstat_loaded_in_last_kiter
# speedup vs baseline: 1.0001x; 1.0001x over previous
; #define PG8_STAGE(bufoff, gbase, voff) do { _Pragma("unroll") for (int _i = 0; _i < 2; ++_i) \
;         __builtin_amdgcn_global_load_lds((const unsigned*)((const char*)(gbase) + (voff)[_i]), (LAS unsigned*)(lds + (bufoff) + ldsw + _i * 8192), 16, 0, 0); } while (0)
; #define PG8_STAGE_A(bufoff, gbase, h, nx) do { if constexpr (GATHER) { unsigned _v[2]; _v[0] = (nx) ? voffAn[h][0] : voffA[h][0]; _v[1] = (nx) ? voffAn[h][1] : voffA[h][1]; PG8_STAGE(bufoff, gbase, _v); } \
;         else PG8_STAGE(bufoff, (gbase) + (h) * hstepA, voffA[0]); } while (0)
; #define PG8_WAIT_V(n) asm volatile("s_waitcnt vmcnt(" #n ")" ::: "memory")
; #define PG8_BAR __builtin_amdgcn_s_barrier()
; template <class Epi, class Sched, bool GATHER, bool ALIGN_EPI>
; __device__ __forceinline__ void gemm_phase(LAS unsigned char* lds, const int wave_, const int K, const int lda, const int ldb, const Sched& S, const Epi& E) {
;     ...
;     for (int i = 0; i < 2; ++i) { int R, C; stage_rc(tid * 16 + i * 8192, R, C); const int Rb = Epi::PERM ? ((R & ~31) + perm32(R & 31)) : R;
;         voffB[i] = (unsigned)(Rb * ldb + C) * 2u; if constexpr (!GATHER) voffA[0][i] = (unsigned)(R * lda + C) * 2u; }
;     const size_t kstep = (size_t)(BK * 2);
;     const size_t hstepB = (size_t)HALF * ldb * 2, hstepA = GATHER ? 0 : (size_t)HALF * lda * 2;
;     const unsigned ldsw = (unsigned)wid * 1024u;
;     const int aoff = lds_byte(wr * 64 + fr, fq * 8), boff = lds_byte(wc * 32 + fr, fq * 8);
;     ...
;     Unit cur, nxt; int ui = 0;
;     if (!S.next(0, cur)) return;
;     PG8_VOFFA(voffA, cur);
;     f32x4 acc[2][2][4][2];
; #pragma unroll
;     for (int a = 0; a < 2; ++a)
; #pragma unroll
;         for (int b = 0; b < 2; ++b)
; #pragma unroll
;             for (int m = 0; m < 4; ++m)
; #pragma unroll
;                 for (int n = 0; n < 2; ++n) acc[a][b][m][n] = (f32x4){0.f, 0.f, 0.f, 0.f};
;     bf16x8 At[4][2], B0[2][2], B1[2][2];
;     const char* cA = cur.A; const char* cB = cur.B;
;     S.a_ready(cur);
;     PG8_STAGE(PG8_SB(0, 0), cB, voffB); PG8_STAGE(PG8_SB(0, 1), cB + hstepB, voffB); PG8_STAGE_A(PG8_SA(0, 0), cA, 0, false); PG8_STAGE_A(PG8_SA(0, 1), cA, 1, false);
;     if (wr == 1) PG8_BAR;
;     PG8_WAIT_V(2); PG8_BAR;
;     PG8_STAGE(PG8_SB(1, 0), cB + kstep, voffB); PG8_STAGE_A(PG8_SA(1, 0), cA + kstep, 0, false); PG8_STAGE(PG8_SB(1, 1), cB + hstepB + kstep, voffB);
;     PG8_WAIT_V(6); PG8_BAR;
.LBB0_710:
	v_and_b32_e32 v15, 15, v14
	v_readlane_b32 s0, v251, 18
	v_bfe_u32 v16, v14, 4, 2
	v_lshlrev_b32_e32 v160, 4, v16
	v_or_b32_e32 v199, s0, v15
	v_lshlrev_b32_e32 v17, 6, v199
	s_movk_i32 s0, 0x3c0
	v_lshlrev_b32_e32 v18, 2, v199
	v_and_or_b32 v17, v17, s0, v160
	v_and_b32_e32 v18, 32, v18
	v_readlane_b32 s0, v251, 19
	v_lshlrev_b32_e32 v14, 2, v14
	v_lshl_add_u64 v[6:7], v[6:7], 0, s[68:69]
	s_add_i32 m0, s22, 0x18000
	v_bitop3_b32 v17, v17, s0, v18 bitop3:0xde
	v_lshl_or_b32 v15, v15, 6, v160
	v_and_b32_e32 v14, 32, v14
	v_readlane_b32 s0, v251, 61
	s_waitcnt vmcnt(2)
	s_barrier
	global_load_lds_dwordx4 v[6:7], off
	v_lshl_add_u64 v[4:5], v[4:5], 0, s[68:69]
	s_add_i32 m0, s22, 0x1a000
	s_add_i32 s26, s22, 0x8000
	s_add_i32 s27, s22, 0xa000
	v_bitop3_b32 v201, v15, s0, v14 bitop3:0xde
	global_load_lds_dwordx4 v[4:5], off
	v_lshl_add_u64 v[0:1], v[0:1], 0, s[68:69]
	s_mov_b32 m0, s26
	s_add_u32 s0, s18, 0x40080
	global_load_lds_dwordx4 v[0:1], off
	v_lshl_add_u64 v[0:1], v[2:3], 0, s[68:69]
	s_mov_b32 m0, s27
	s_addc_u32 s1, s19, 0
	global_load_lds_dwordx4 v[0:1], off
	v_lshl_add_u64 v[0:1], s[0:1], 0, v[156:157]
	s_add_i32 m0, s22, 0x1c000
	v_readlane_b32 s2, v251, 32
	global_load_lds_dwordx4 v[0:1], off
	v_lshl_add_u64 v[0:1], s[0:1], 0, v[162:163]
	s_add_i32 m0, s22, 0x1e000
	v_readlane_b32 s3, v251, 33
	v_readlane_b32 s100, v251, 32
	v_readlane_b32 s101, v251, 33
	global_load_lds_dwordx4 v[0:1], off
	v_lshlrev_b32_e32 v0, 14, v8
	v_and_b32_e32 v0, 0xffff8000, v0
	v_lshl_add_u32 v0, v9, 11, v0
	v_and_b32_e32 v1, 1, v8
	v_lshl_or_b32 v0, v1, 6, v0
	v_lshl_add_u64 v[166:167], s[2:3], 0, v[160:161]
	v_readlane_b32 s2, v251, 28
	v_lshl_add_u32 v172, v10, 1, v0
	v_lshlrev_b32_e32 v0, 14, v11
	v_readlane_b32 s0, v251, 60
	v_readlane_b32 s3, v251, 29
	v_and_b32_e32 v0, 0xffff8000, v0
	s_waitcnt vmcnt(6)
	v_lshl_or_b32 v203, v16, 3, s0
	v_readlane_b32 s0, v253, 5
	v_lshl_add_u64 v[168:169], s[2:3], 0, v[160:161]
	v_readlane_b32 s2, v251, 30
	v_lshl_add_u32 v0, v12, 11, v0
	v_and_b32_e32 v1, 1, v11
	v_cmp_gt_u32_e32 vcc, 2, v16
	v_readlane_b32 s1, v253, 6
	v_readlane_b32 s3, v251, 31
	v_lshl_or_b32 v0, v1, 6, v0
	v_or_b32_e32 v213, 0xfffff400, v203
	v_or_b32_e32 v214, 0xfffff800, v203
	s_and_b64 s[0:1], s[0:1], vcc
	v_lshl_add_u64 v[170:171], s[2:3], 0, v[160:161]
	v_mov_b32_e32 v173, v161
	v_lshl_add_u32 v174, v13, 1, v0
	v_mov_b32_e32 v175, v161
	s_mov_b32 s28, 0
	v_add_u32_e32 v215, 0, v17
	s_mov_b64 s[14:15], s[4:5]
	s_mov_b64 s[16:17], s[18:19]
	s_barrier
	s_branch .LBB0_713

; #define PG8_STAGE(bufoff, gbase, voff) do { _Pragma("unroll") for (int _i = 0; _i < 2; ++_i) \
;         __builtin_amdgcn_global_load_lds((const unsigned*)((const char*)(gbase) + (voff)[_i]), (LAS unsigned*)(lds + (bufoff) + ldsw + _i * 8192), 16, 0, 0); } while (0)
; #define PG8_STAGE_A(bufoff, gbase, h, nx) do { if constexpr (GATHER) { unsigned _v[2]; _v[0] = (nx) ? voffAn[h][0] : voffA[h][0]; _v[1] = (nx) ? voffAn[h][1] : voffA[h][1]; PG8_STAGE(bufoff, gbase, _v); } \
;         else PG8_STAGE(bufoff, (gbase) + (h) * hstepA, voffA[0]); } while (0)
; #define PG8_LDA(dst, b, h) do { _Pragma("unroll") for (int m = 0; m < 4; ++m) _Pragma("unroll") for (int k = 0; k < 2; ++k) dst[m][k] = *(const LAS bf16x8*)(lds + PG8_SA(b, h) + aoff + m * 2048 + k * 1024); } while (0)
; #define PG8_LDB(dst, b, h) do { _Pragma("unroll") for (int n = 0; n < 2; ++n) _Pragma("unroll") for (int k = 0; k < 2; ++k) dst[n][k] = *(const LAS bf16x8*)(lds + PG8_SB(b, h) + boff + n * 2048 + k * 1024); } while (0)
; #define PG8_BAR __builtin_amdgcn_s_barrier()
; template <class Epi, class Sched, bool GATHER, bool ALIGN_EPI>
; __device__ __forceinline__ void gemm_phase(LAS unsigned char* lds, const int wave_, const int K, const int lda, const int ldb, const Sched& S, const Epi& E) {
;     ...
;     f32x4 acc[2][2][4][2];
; #pragma unroll
;     for (int a = 0; a < 2; ++a)
; #pragma unroll
;         for (int b = 0; b < 2; ++b)
; #pragma unroll
;             for (int m = 0; m < 4; ++m)
; #pragma unroll
;                 for (int n = 0; n < 2; ++n) acc[a][b][m][n] = (f32x4){0.f, 0.f, 0.f, 0.f};
;     ...
;         for (int t = 0; t < nt; t += 2) {
;             const bool last = (t == nt - 2);
;             const char* a1 = cA + (size_t)(t + 1) * kstep;
;             const char* a2 = last ? nA : cA + (size_t)(t + 2) * kstep; const char* b2 = last ? nB : cB + (size_t)(t + 2) * kstep;
;             const char* a3 = a2 + kstep; const char* b3 = b2 + kstep;
;             if (last && has_next) S.a_ready(nxt);
;             PG8_LDB(B0, 0, 0); PG8_LDB(B1, 0, 1); PG8_SCHED; PG8_LDA(At, 0, 0); PG8_STAGE_A(PG8_SA(1, 1), a1, 1, false);
;             PG8_WAIT_V(8); PG8_WAIT_L(0); PG8_BAR; PG8_MMA(0, 0, At, B0); PG8_MMA(0, 1, At, B1); PG8_BAR; PG8_SCHED;
;             PG8_LDA(At, 0, 1); PG8_STAGE(PG8_SB(0, 0), b2, voffB); PG8_STAGE(PG8_SB(0, 1), b2 + hstepB, voffB); PG8_STAGE_A(PG8_SA(0, 0), a2, 0, last);
.LBB0_719:
	v_lshl_add_u32 v244, s30, 8, v199
	v_lshlrev_b32_e32 v244, 6, v244
	v_add_u32_e32 v245, 0x2000, v244
	s_add_u32 s4, s4, 0x40080
	s_addc_u32 s5, s5, 0
	s_add_u32 s11, s18, 0x100
	v_mov_b32_e32 v0, 0
	v_mov_b64_e32 v[210:211], 0xff
	s_addc_u32 s13, s19, 0
	s_mov_b32 s31, -2
	v_mov_b32_e32 v1, v0
	v_mov_b32_e32 v2, v0
	v_mov_b32_e32 v3, v0
	v_mov_b32_e32 v4, v0
	v_mov_b32_e32 v5, v0
	v_mov_b32_e32 v6, v0
	v_mov_b32_e32 v7, v0
	v_mov_b32_e32 v16, v0
	v_mov_b32_e32 v17, v0
	v_mov_b32_e32 v18, v0
	v_mov_b32_e32 v19, v0
	v_mov_b32_e32 v20, v0
	v_mov_b32_e32 v21, v0
	v_mov_b32_e32 v22, v0
	v_mov_b32_e32 v23, v0
	v_mov_b32_e32 v32, v0
	v_mov_b32_e32 v33, v0
	v_mov_b32_e32 v34, v0
	v_mov_b32_e32 v35, v0
	v_mov_b32_e32 v36, v0
	v_mov_b32_e32 v37, v0
	v_mov_b32_e32 v38, v0
	v_mov_b32_e32 v39, v0
	v_mov_b32_e32 v48, v0
	v_mov_b32_e32 v49, v0
	v_mov_b32_e32 v50, v0
	v_mov_b32_e32 v51, v0
	v_mov_b32_e32 v52, v0
	v_mov_b32_e32 v53, v0
	v_mov_b32_e32 v54, v0
	v_mov_b32_e32 v55, v0
	v_mov_b32_e32 v8, v0
	v_mov_b32_e32 v9, v0
	v_mov_b32_e32 v10, v0
	v_mov_b32_e32 v11, v0
	v_mov_b32_e32 v12, v0
	v_mov_b32_e32 v13, v0
	v_mov_b32_e32 v14, v0
	v_mov_b32_e32 v15, v0
	v_mov_b32_e32 v24, v0
	v_mov_b32_e32 v25, v0
	v_mov_b32_e32 v26, v0
	v_mov_b32_e32 v27, v0
	v_mov_b32_e32 v28, v0
	v_mov_b32_e32 v29, v0
	v_mov_b32_e32 v30, v0
	v_mov_b32_e32 v31, v0
	v_mov_b32_e32 v40, v0
	v_mov_b32_e32 v41, v0
	v_mov_b32_e32 v42, v0
	v_mov_b32_e32 v43, v0
	v_mov_b32_e32 v44, v0
	v_mov_b32_e32 v45, v0
	v_mov_b32_e32 v46, v0
	v_mov_b32_e32 v47, v0
	v_mov_b32_e32 v56, v0
	v_mov_b32_e32 v57, v0
	v_mov_b32_e32 v58, v0
	v_mov_b32_e32 v59, v0
	v_mov_b32_e32 v60, v0
	v_mov_b32_e32 v61, v0
	v_mov_b32_e32 v62, v0
	v_mov_b32_e32 v63, v0
	v_mov_b32_e32 v64, v0
	v_mov_b32_e32 v65, v0
	v_mov_b32_e32 v66, v0
	v_mov_b32_e32 v67, v0
	v_mov_b32_e32 v68, v0
	v_mov_b32_e32 v69, v0
	v_mov_b32_e32 v70, v0
	v_mov_b32_e32 v71, v0
	v_mov_b32_e32 v80, v0
	v_mov_b32_e32 v81, v0
	v_mov_b32_e32 v82, v0
	v_mov_b32_e32 v83, v0
	v_mov_b32_e32 v84, v0
	v_mov_b32_e32 v85, v0
	v_mov_b32_e32 v86, v0
	v_mov_b32_e32 v87, v0
	v_mov_b32_e32 v96, v0
	v_mov_b32_e32 v97, v0
	v_mov_b32_e32 v98, v0
	v_mov_b32_e32 v99, v0
	v_mov_b32_e32 v100, v0
	v_mov_b32_e32 v101, v0
	v_mov_b32_e32 v102, v0
	v_mov_b32_e32 v103, v0
	v_mov_b32_e32 v112, v0
	v_mov_b32_e32 v113, v0
	v_mov_b32_e32 v114, v0
	v_mov_b32_e32 v115, v0
	v_mov_b32_e32 v116, v0
	v_mov_b32_e32 v117, v0
	v_mov_b32_e32 v118, v0
	v_mov_b32_e32 v119, v0
	v_mov_b32_e32 v72, v0
	v_mov_b32_e32 v73, v0
	v_mov_b32_e32 v74, v0
	v_mov_b32_e32 v75, v0
	v_mov_b32_e32 v76, v0
	v_mov_b32_e32 v77, v0
	v_mov_b32_e32 v78, v0
	v_mov_b32_e32 v79, v0
	v_mov_b32_e32 v88, v0
	v_mov_b32_e32 v89, v0
	v_mov_b32_e32 v90, v0
	v_mov_b32_e32 v91, v0
	v_mov_b32_e32 v92, v0
	v_mov_b32_e32 v93, v0
	v_mov_b32_e32 v94, v0
	v_mov_b32_e32 v95, v0
	v_mov_b32_e32 v104, v0
	v_mov_b32_e32 v105, v0
	v_mov_b32_e32 v106, v0
	v_mov_b32_e32 v107, v0
	v_mov_b32_e32 v108, v0
	v_mov_b32_e32 v109, v0
	v_mov_b32_e32 v110, v0
	v_mov_b32_e32 v111, v0
	v_mov_b32_e32 v120, v0
	v_mov_b32_e32 v121, v0
	v_mov_b32_e32 v122, v0
	v_mov_b32_e32 v123, v0
	v_mov_b32_e32 v124, v0
	v_mov_b32_e32 v125, v0
	v_mov_b32_e32 v126, v0
	v_mov_b32_e32 v127, v0
.LBB0_720:
	s_add_u32 s2, s4, 0xfffc0080
	s_addc_u32 s3, s5, -1
	s_cmp_eq_u32 s31, 12
	s_cselect_b32 s21, s15, s3
	s_cselect_b32 s20, s14, s2
	s_cselect_b32 s19, s17, s13
	s_cselect_b32 s18, s16, s11
	s_add_i32 s2, 0, 0x10000
	s_add_i32 s8, 0, 0x14000
	v_add_u32_e32 v140, s2, v201
	v_add_u32_e32 v160, s8, v201
	ds_read_b128 v[128:131], v140
	ds_read_b128 v[132:135], v140 offset:1024
	ds_read_b128 v[136:139], v140 offset:2048
	ds_read_b128 v[140:143], v140 offset:3072
	ds_read_b128 v[144:147], v160
	ds_read_b128 v[148:151], v160 offset:1024
	ds_read_b128 v[152:155], v160 offset:2048
	ds_read_b128 v[176:179], v160 offset:3072
	v_lshl_add_u64 v[188:189], s[4:5], 0, v[172:173]
	s_add_i32 m0, s22, 0xc000
	ds_read_b128 v[180:183], v215
	ds_read_b128 v[184:187], v215 offset:1024
	ds_read_b128 v[204:207], v215 offset:2048
	ds_read_b128 v[216:219], v215 offset:3072
	ds_read_b128 v[220:223], v215 offset:4096
	ds_read_b128 v[224:227], v215 offset:5120
	ds_read_b128 v[228:231], v215 offset:6144
	ds_read_b128 v[232:235], v215 offset:7168
	global_load_lds_dwordx4 v[188:189], off
	v_lshl_add_u64 v[188:189], s[4:5], 0, v[174:175]
	s_add_i32 m0, s22, 0xe000
	s_nop 0
	global_load_lds_dwordx4 v[188:189], off
	s_waitcnt vmcnt(8)
	s_waitcnt lgkmcnt(0)
	s_barrier
; #define PG8_STAGE(bufoff, gbase, voff) do { _Pragma("unroll") for (int _i = 0; _i < 2; ++_i) \
;         __builtin_amdgcn_global_load_lds((const unsigned*)((const char*)(gbase) + (voff)[_i]), (LAS unsigned*)(lds + (bufoff) + ldsw + _i * 8192), 16, 0, 0); } while (0)
; #define PG8_STAGE_A(bufoff, gbase, h, nx) do { if constexpr (GATHER) { unsigned _v[2]; _v[0] = (nx) ? voffAn[h][0] : voffA[h][0]; _v[1] = (nx) ? voffAn[h][1] : voffA[h][1]; PG8_STAGE(bufoff, gbase, _v); } \
;         else PG8_STAGE(bufoff, (gbase) + (h) * hstepA, voffA[0]); } while (0)
; #define PG8_LDA(dst, b, h) do { _Pragma("unroll") for (int m = 0; m < 4; ++m) _Pragma("unroll") for (int k = 0; k < 2; ++k) dst[m][k] = *(const LAS bf16x8*)(lds + PG8_SA(b, h) + aoff + m * 2048 + k * 1024); } while (0)
; #define PG8_LDB(dst, b, h) do { _Pragma("unroll") for (int n = 0; n < 2; ++n) _Pragma("unroll") for (int k = 0; k < 2; ++k) dst[n][k] = *(const LAS bf16x8*)(lds + PG8_SB(b, h) + boff + n * 2048 + k * 1024); } while (0)
; #define PG8_WAIT_V(n) asm volatile("s_waitcnt vmcnt(" #n ")" ::: "memory")
; #define PG8_WAIT_L(n) asm volatile("s_waitcnt lgkmcnt(" #n ")" ::: "memory")
; __device__ __forceinline__ void row_rscale8(const float* part, const int (&rows)[2][4], int fq, float (&rs)[2][4]) {
;     ...
;         for (int m = 0; m < 4; ++m) v[ai][m] = *(const f32x4*)(part + (size_t)rows[ai][m] * 16 + fq * 4);
; template <class Epi, class Sched, bool GATHER, bool ALIGN_EPI>
; __device__ __forceinline__ void gemm_phase(LAS unsigned char* lds, const int wave_, const int K, const int lda, const int ldb, const Sched& S, const Epi& E) {
;     ...
;             PG8_LDB(B0, 0, 0); PG8_LDB(B1, 0, 1); PG8_SCHED; PG8_LDA(At, 0, 0); PG8_STAGE_A(PG8_SA(1, 1), a1, 1, false);
;             PG8_WAIT_V(8); PG8_WAIT_L(0); PG8_BAR; PG8_MMA(0, 0, At, B0); PG8_MMA(0, 1, At, B1); PG8_BAR; PG8_SCHED;
;             PG8_LDA(At, 0, 1); PG8_STAGE(PG8_SB(0, 0), b2, voffB); PG8_STAGE(PG8_SB(0, 1), b2 + hstepB, voffB); PG8_STAGE_A(PG8_SA(0, 0), a2, 0, last);
;             PG8_WAIT_V(8); PG8_WAIT_L(0); PG8_BAR; PG8_MMA(1, 0, At, B0); PG8_MMA(1, 1, At, B1); PG8_BAR; PG8_SCHED;
;             PG8_LDB(B0, 1, 0); PG8_LDB(B1, 1, 1); PG8_SCHED; PG8_LDA(At, 1, 0); PG8_STAGE_A(PG8_SA(0, 1), a2, 1, last);
;             PG8_WAIT_V(8); PG8_WAIT_L(0); PG8_BAR; PG8_MMA(0, 0, At, B0); PG8_MMA(0, 1, At, B1); PG8_BAR; PG8_SCHED;
	s_setprio 1
	s_waitcnt lgkmcnt(0)
	v_mfma_f32_16x16x32_bf16 v[124:127], v[128:131], v[180:183], v[124:127]
	v_mfma_f32_16x16x32_bf16 v[120:123], v[136:139], v[180:183], v[120:123]
	v_mfma_f32_16x16x32_bf16 v[108:111], v[128:131], v[204:207], v[108:111]
	v_mfma_f32_16x16x32_bf16 v[104:107], v[136:139], v[204:207], v[104:107]
	v_mfma_f32_16x16x32_bf16 v[92:95], v[128:131], v[220:223], v[92:95]
	v_mfma_f32_16x16x32_bf16 v[88:91], v[136:139], v[220:223], v[88:91]
	v_mfma_f32_16x16x32_bf16 v[76:79], v[128:131], v[228:231], v[76:79]
	v_mfma_f32_16x16x32_bf16 v[72:75], v[136:139], v[228:231], v[72:75]
	v_mfma_f32_16x16x32_bf16 v[124:127], v[132:135], v[184:187], v[124:127]
	v_mfma_f32_16x16x32_bf16 v[120:123], v[140:143], v[184:187], v[120:123]
	v_mfma_f32_16x16x32_bf16 v[108:111], v[132:135], v[216:219], v[108:111]
	v_mfma_f32_16x16x32_bf16 v[104:107], v[140:143], v[216:219], v[104:107]
	v_mfma_f32_16x16x32_bf16 v[92:95], v[132:135], v[224:227], v[92:95]
	v_mfma_f32_16x16x32_bf16 v[88:91], v[140:143], v[224:227], v[88:91]
	v_mfma_f32_16x16x32_bf16 v[76:79], v[132:135], v[232:235], v[76:79]
	v_mfma_f32_16x16x32_bf16 v[72:75], v[140:143], v[232:235], v[72:75]
	s_setprio 0
	s_setprio 1
	v_mfma_f32_16x16x32_bf16 v[116:119], v[144:147], v[180:183], v[116:119]
	v_mfma_f32_16x16x32_bf16 v[112:115], v[152:155], v[180:183], v[112:115]
	v_mfma_f32_16x16x32_bf16 v[100:103], v[144:147], v[204:207], v[100:103]
	v_mfma_f32_16x16x32_bf16 v[96:99], v[152:155], v[204:207], v[96:99]
	v_mfma_f32_16x16x32_bf16 v[84:87], v[144:147], v[220:223], v[84:87]
	v_mfma_f32_16x16x32_bf16 v[80:83], v[152:155], v[220:223], v[80:83]
	v_mfma_f32_16x16x32_bf16 v[68:71], v[144:147], v[228:231], v[68:71]
	v_mfma_f32_16x16x32_bf16 v[64:67], v[152:155], v[228:231], v[64:67]
	v_mfma_f32_16x16x32_bf16 v[116:119], v[148:151], v[184:187], v[116:119]
	v_mfma_f32_16x16x32_bf16 v[112:115], v[176:179], v[184:187], v[112:115]
	v_mfma_f32_16x16x32_bf16 v[100:103], v[148:151], v[216:219], v[100:103]
	v_mfma_f32_16x16x32_bf16 v[96:99], v[176:179], v[216:219], v[96:99]
	v_mfma_f32_16x16x32_bf16 v[84:87], v[148:151], v[224:227], v[84:87]
	v_mfma_f32_16x16x32_bf16 v[80:83], v[176:179], v[224:227], v[80:83]
	v_mfma_f32_16x16x32_bf16 v[68:71], v[148:151], v[232:235], v[68:71]
	v_mfma_f32_16x16x32_bf16 v[64:67], v[176:179], v[232:235], v[64:67]
	s_setprio 0
	s_barrier
	s_add_i32 s2, s2, s62
	v_lshl_add_u64 v[188:189], s[18:19], 0, v[156:157]
	s_mov_b32 m0, s2
	ds_read_b128 v[180:183], v215 offset:16384
	ds_read_b128 v[184:187], v215 offset:17408
	ds_read_b128 v[204:207], v215 offset:18432
	ds_read_b128 v[216:219], v215 offset:19456
	ds_read_b128 v[220:223], v215 offset:20480
	ds_read_b128 v[224:227], v215 offset:21504
	ds_read_b128 v[228:231], v215 offset:22528
	ds_read_b128 v[232:235], v215 offset:23552
	global_load_lds_dwordx4 v[188:189], off
	s_add_i32 m0, s2, 0x2000
	s_add_u32 s2, s18, 0x40000
	v_lshl_add_u64 v[190:191], s[18:19], 0, v[162:163]
	s_addc_u32 s3, s19, 0
	s_add_i32 s8, s8, s62
	global_load_lds_dwordx4 v[190:191], off
	v_lshl_add_u64 v[192:193], s[2:3], 0, v[156:157]
	s_mov_b32 m0, s8
	v_lshl_add_u64 v[196:197], s[20:21], 0, v[164:165]
	global_load_lds_dwordx4 v[192:193], off
	v_lshl_add_u64 v[192:193], s[2:3], 0, v[162:163]
	s_add_i32 m0, s8, 0x2000
	s_nop 0
	global_load_lds_dwordx4 v[192:193], off
	v_lshl_add_u64 v[192:193], s[20:21], 0, v[158:159]
	s_mov_b32 m0, s22
	s_nop 0
	global_load_lds_dwordx4 v[192:193], off
	s_mov_b32 m0, s23
	s_nop 0
	global_load_lds_dwordx4 v[196:197], off
	s_waitcnt vmcnt(8)
	s_waitcnt lgkmcnt(0)
	s_barrier
	s_setprio 1
	s_waitcnt lgkmcnt(0)
	v_mfma_f32_16x16x32_bf16 v[60:63], v[128:131], v[180:183], v[60:63]
	v_mfma_f32_16x16x32_bf16 v[56:59], v[136:139], v[180:183], v[56:59]
	v_mfma_f32_16x16x32_bf16 v[44:47], v[128:131], v[204:207], v[44:47]
	v_mfma_f32_16x16x32_bf16 v[40:43], v[136:139], v[204:207], v[40:43]
	v_mfma_f32_16x16x32_bf16 v[28:31], v[128:131], v[220:223], v[28:31]
	v_mfma_f32_16x16x32_bf16 v[24:27], v[136:139], v[220:223], v[24:27]
	v_mfma_f32_16x16x32_bf16 v[12:15], v[128:131], v[228:231], v[12:15]
	v_mfma_f32_16x16x32_bf16 v[8:11], v[136:139], v[228:231], v[8:11]
	v_mfma_f32_16x16x32_bf16 v[60:63], v[132:135], v[184:187], v[60:63]
	v_mfma_f32_16x16x32_bf16 v[56:59], v[140:143], v[184:187], v[56:59]
	v_mfma_f32_16x16x32_bf16 v[44:47], v[132:135], v[216:219], v[44:47]
	v_mfma_f32_16x16x32_bf16 v[40:43], v[140:143], v[216:219], v[40:43]
	v_mfma_f32_16x16x32_bf16 v[28:31], v[132:135], v[224:227], v[28:31]
	v_mfma_f32_16x16x32_bf16 v[24:27], v[140:143], v[224:227], v[24:27]
	v_mfma_f32_16x16x32_bf16 v[12:15], v[132:135], v[232:235], v[12:15]
	v_mfma_f32_16x16x32_bf16 v[8:11], v[140:143], v[232:235], v[8:11]
	s_setprio 0
	s_setprio 1
	v_mfma_f32_16x16x32_bf16 v[52:55], v[144:147], v[180:183], v[52:55]
	v_mfma_f32_16x16x32_bf16 v[48:51], v[152:155], v[180:183], v[48:51]
	v_mfma_f32_16x16x32_bf16 v[36:39], v[144:147], v[204:207], v[36:39]
	v_mfma_f32_16x16x32_bf16 v[32:35], v[152:155], v[204:207], v[32:35]
	v_mfma_f32_16x16x32_bf16 v[20:23], v[144:147], v[220:223], v[20:23]
	v_mfma_f32_16x16x32_bf16 v[16:19], v[152:155], v[220:223], v[16:19]
	v_mfma_f32_16x16x32_bf16 v[4:7], v[144:147], v[228:231], v[4:7]
	v_mfma_f32_16x16x32_bf16 v[0:3], v[152:155], v[228:231], v[0:3]
	v_mfma_f32_16x16x32_bf16 v[52:55], v[148:151], v[184:187], v[52:55]
	v_mfma_f32_16x16x32_bf16 v[48:51], v[176:179], v[184:187], v[48:51]
	v_mfma_f32_16x16x32_bf16 v[36:39], v[148:151], v[216:219], v[36:39]
	v_mfma_f32_16x16x32_bf16 v[32:35], v[176:179], v[216:219], v[32:35]
	v_mfma_f32_16x16x32_bf16 v[20:23], v[148:151], v[224:227], v[20:23]
	v_mfma_f32_16x16x32_bf16 v[16:19], v[176:179], v[224:227], v[16:19]
	v_mfma_f32_16x16x32_bf16 v[4:7], v[148:151], v[232:235], v[4:7]
	v_mfma_f32_16x16x32_bf16 v[0:3], v[176:179], v[232:235], v[0:3]
	s_setprio 0
	s_barrier
	s_cmp_eq_u32 s31, 12
	s_cbranch_scc0 .Lin_part_skip
	global_load_dword v236, v244, s[100:101]
	global_load_dword v237, v244, s[100:101] offset:1024
	global_load_dword v238, v244, s[100:101] offset:2048
	global_load_dword v239, v244, s[100:101] offset:3072
	global_load_dword v240, v245, s[100:101]
	global_load_dword v241, v245, s[100:101] offset:1024
	global_load_dword v242, v245, s[100:101] offset:2048
	global_load_dword v243, v245, s[100:101] offset:3072
; #define PG8_STAGE(bufoff, gbase, voff) do { _Pragma("unroll") for (int _i = 0; _i < 2; ++_i) \
;         __builtin_amdgcn_global_load_lds((const unsigned*)((const char*)(gbase) + (voff)[_i]), (LAS unsigned*)(lds + (bufoff) + ldsw + _i * 8192), 16, 0, 0); } while (0)
; #define PG8_STAGE_A(bufoff, gbase, h, nx) do { if constexpr (GATHER) { unsigned _v[2]; _v[0] = (nx) ? voffAn[h][0] : voffA[h][0]; _v[1] = (nx) ? voffAn[h][1] : voffA[h][1]; PG8_STAGE(bufoff, gbase, _v); } \
;         else PG8_STAGE(bufoff, (gbase) + (h) * hstepA, voffA[0]); } while (0)
; #define PG8_LDA(dst, b, h) do { _Pragma("unroll") for (int m = 0; m < 4; ++m) _Pragma("unroll") for (int k = 0; k < 2; ++k) dst[m][k] = *(const LAS bf16x8*)(lds + PG8_SA(b, h) + aoff + m * 2048 + k * 1024); } while (0)
; #define PG8_LDB(dst, b, h) do { _Pragma("unroll") for (int n = 0; n < 2; ++n) _Pragma("unroll") for (int k = 0; k < 2; ++k) dst[n][k] = *(const LAS bf16x8*)(lds + PG8_SB(b, h) + boff + n * 2048 + k * 1024); } while (0)
; #define PG8_MMA(ai, bj, At, Bt) do { __builtin_amdgcn_s_setprio(1); _Pragma("unroll") for (int m = 0; m < 4; ++m) _Pragma("unroll") for (int n = 0; n < 2; ++n) _Pragma("unroll") for (int k = 0; k < 2; ++k) \
;         acc[ai][bj][m][n] = __builtin_amdgcn_mfma_f32_16x16x32_bf16(Bt[n][k], At[m][k], acc[ai][bj][m][n], 0, 0, 0); __builtin_amdgcn_s_setprio(0); } while (0)
; #define PG8_WAIT_V(n) asm volatile("s_waitcnt vmcnt(" #n ")" ::: "memory")
; #define PG8_WAIT_L(n) asm volatile("s_waitcnt lgkmcnt(" #n ")" ::: "memory")
; #define PG8_BAR __builtin_amdgcn_s_barrier()
; #define PG8_SCHED __builtin_amdgcn_sched_barrier(0)
; template <class Epi, class Sched, bool GATHER, bool ALIGN_EPI>
; __device__ __forceinline__ void gemm_phase(LAS unsigned char* lds, const int wave_, const int K, const int lda, const int ldb, const Sched& S, const Epi& E) {
;     ...
;             PG8_LDB(B0, 1, 0); PG8_LDB(B1, 1, 1); PG8_SCHED; PG8_LDA(At, 1, 0); PG8_STAGE_A(PG8_SA(0, 1), a2, 1, last);
;             PG8_WAIT_V(8); PG8_WAIT_L(0); PG8_BAR; PG8_MMA(0, 0, At, B0); PG8_MMA(0, 1, At, B1); PG8_BAR; PG8_SCHED;
;             PG8_LDA(At, 1, 1); PG8_STAGE(PG8_SB(1, 0), b3, voffB); PG8_STAGE(PG8_SB(1, 1), b3 + hstepB, voffB); PG8_STAGE_A(PG8_SA(1, 0), a3, 0, last);
;             PG8_WAIT_V(8); PG8_WAIT_L(0); PG8_BAR; PG8_MMA(1, 0, At, B0); PG8_MMA(1, 1, At, B1); PG8_BAR; PG8_SCHED;
.Lin_part_skip:
	s_add_i32 s8, 0, 0x18000
	s_add_i32 s9, 0, 0x1c000
	v_add_u32_e32 v140, s8, v201
	v_add_u32_e32 v160, s9, v201
	ds_read_b128 v[128:131], v140
	ds_read_b128 v[132:135], v140 offset:1024
	ds_read_b128 v[136:139], v140 offset:2048
	ds_read_b128 v[140:143], v140 offset:3072
	ds_read_b128 v[144:147], v160
	ds_read_b128 v[148:151], v160 offset:1024
	ds_read_b128 v[152:155], v160 offset:2048
	ds_read_b128 v[176:179], v160 offset:3072
	s_add_u32 s2, s20, 0x40000
	s_addc_u32 s3, s21, 0
	s_mov_b32 m0, s24
	v_lshl_add_u64 v[208:209], s[2:3], 0, v[158:159]
	ds_read_b128 v[180:183], v215 offset:32768
	ds_read_b128 v[184:187], v215 offset:33792
	ds_read_b128 v[204:207], v215 offset:34816
	ds_read_b128 v[216:219], v215 offset:35840
	ds_read_b128 v[220:223], v215 offset:36864
	ds_read_b128 v[224:227], v215 offset:37888
	ds_read_b128 v[228:231], v215 offset:38912
	ds_read_b128 v[232:235], v215 offset:39936
	global_load_lds_dwordx4 v[208:209], off
	v_lshl_add_u64 v[208:209], s[2:3], 0, v[164:165]
	s_mov_b32 m0, s25
	s_nop 0
	global_load_lds_dwordx4 v[208:209], off
	s_cmp_eq_u32 s31, 12
	s_cbranch_scc1 .Lin_part_w16
	s_waitcnt vmcnt(8)
	s_branch .Lin_part_wd
.Lin_part_w16:
	s_waitcnt vmcnt(16)
.Lin_part_wd:
	s_waitcnt lgkmcnt(0)
	s_barrier
	s_setprio 1
	s_waitcnt lgkmcnt(0)
	v_mfma_f32_16x16x32_bf16 v[124:127], v[128:131], v[180:183], v[124:127]
	v_mfma_f32_16x16x32_bf16 v[120:123], v[136:139], v[180:183], v[120:123]
	v_mfma_f32_16x16x32_bf16 v[108:111], v[128:131], v[204:207], v[108:111]
	v_mfma_f32_16x16x32_bf16 v[104:107], v[136:139], v[204:207], v[104:107]
	v_mfma_f32_16x16x32_bf16 v[92:95], v[128:131], v[220:223], v[92:95]
	v_mfma_f32_16x16x32_bf16 v[88:91], v[136:139], v[220:223], v[88:91]
	v_mfma_f32_16x16x32_bf16 v[76:79], v[128:131], v[228:231], v[76:79]
	v_mfma_f32_16x16x32_bf16 v[72:75], v[136:139], v[228:231], v[72:75]
	v_mfma_f32_16x16x32_bf16 v[124:127], v[132:135], v[184:187], v[124:127]
	v_mfma_f32_16x16x32_bf16 v[120:123], v[140:143], v[184:187], v[120:123]
	v_mfma_f32_16x16x32_bf16 v[108:111], v[132:135], v[216:219], v[108:111]
	v_mfma_f32_16x16x32_bf16 v[104:107], v[140:143], v[216:219], v[104:107]
	v_mfma_f32_16x16x32_bf16 v[92:95], v[132:135], v[224:227], v[92:95]
	v_mfma_f32_16x16x32_bf16 v[88:91], v[140:143], v[224:227], v[88:91]
	v_mfma_f32_16x16x32_bf16 v[76:79], v[132:135], v[232:235], v[76:79]
	v_mfma_f32_16x16x32_bf16 v[72:75], v[140:143], v[232:235], v[72:75]
	s_setprio 0
	s_setprio 1
	v_mfma_f32_16x16x32_bf16 v[116:119], v[144:147], v[180:183], v[116:119]
	v_mfma_f32_16x16x32_bf16 v[112:115], v[152:155], v[180:183], v[112:115]
	v_mfma_f32_16x16x32_bf16 v[100:103], v[144:147], v[204:207], v[100:103]
	v_mfma_f32_16x16x32_bf16 v[96:99], v[152:155], v[204:207], v[96:99]
	v_mfma_f32_16x16x32_bf16 v[84:87], v[144:147], v[220:223], v[84:87]
	v_mfma_f32_16x16x32_bf16 v[80:83], v[152:155], v[220:223], v[80:83]
	v_mfma_f32_16x16x32_bf16 v[68:71], v[144:147], v[228:231], v[68:71]
	v_mfma_f32_16x16x32_bf16 v[64:67], v[152:155], v[228:231], v[64:67]
	v_mfma_f32_16x16x32_bf16 v[116:119], v[148:151], v[184:187], v[116:119]
	v_mfma_f32_16x16x32_bf16 v[112:115], v[176:179], v[184:187], v[112:115]
	v_mfma_f32_16x16x32_bf16 v[100:103], v[148:151], v[216:219], v[100:103]
	v_mfma_f32_16x16x32_bf16 v[96:99], v[176:179], v[216:219], v[96:99]
	v_mfma_f32_16x16x32_bf16 v[84:87], v[148:151], v[224:227], v[84:87]
	v_mfma_f32_16x16x32_bf16 v[80:83], v[176:179], v[224:227], v[80:83]
	v_mfma_f32_16x16x32_bf16 v[68:71], v[148:151], v[232:235], v[68:71]
	v_mfma_f32_16x16x32_bf16 v[64:67], v[176:179], v[232:235], v[64:67]
	s_setprio 0
	s_barrier
	s_add_i32 s2, s8, s62
	v_lshl_add_u64 v[188:189], v[188:189], 0, s[68:69]
	s_mov_b32 m0, s2
	ds_read_b128 v[180:183], v215 offset:49152
	ds_read_b128 v[184:187], v215 offset:50176
	ds_read_b128 v[204:207], v215 offset:51200
	ds_read_b128 v[216:219], v215 offset:52224
	ds_read_b128 v[220:223], v215 offset:53248
	ds_read_b128 v[224:227], v215 offset:54272
	ds_read_b128 v[228:231], v215 offset:55296
	ds_read_b128 v[232:235], v215 offset:56320
	global_load_lds_dwordx4 v[188:189], off
	s_add_i32 m0, s2, 0x2000
	s_add_u32 s2, s18, 0x40080
	v_lshl_add_u64 v[188:189], v[190:191], 0, s[68:69]
	s_addc_u32 s3, s19, 0
	s_add_i32 s8, s9, s62
	global_load_lds_dwordx4 v[188:189], off
	v_lshl_add_u64 v[188:189], s[2:3], 0, v[156:157]
	s_mov_b32 m0, s8
	s_nop 0
	global_load_lds_dwordx4 v[188:189], off
	v_lshl_add_u64 v[188:189], s[2:3], 0, v[162:163]
	s_add_i32 m0, s8, 0x2000
	s_nop 0
	global_load_lds_dwordx4 v[188:189], off
	v_lshl_add_u64 v[188:189], v[192:193], 0, s[68:69]
	s_mov_b32 m0, s26
	s_nop 0
	global_load_lds_dwordx4 v[188:189], off
	v_lshl_add_u64 v[188:189], v[196:197], 0, s[68:69]
	s_mov_b32 m0, s27
	s_nop 0
	global_load_lds_dwordx4 v[188:189], off
	s_waitcnt vmcnt(8)
	s_waitcnt lgkmcnt(0)
	s_barrier
; #define PG8_STAGE(bufoff, gbase, voff) do { _Pragma("unroll") for (int _i = 0; _i < 2; ++_i) \
;         __builtin_amdgcn_global_load_lds((const unsigned*)((const char*)(gbase) + (voff)[_i]), (LAS unsigned*)(lds + (bufoff) + ldsw + _i * 8192), 16, 0, 0); } while (0)
; #define PG8_STAGE_A(bufoff, gbase, h, nx) do { if constexpr (GATHER) { unsigned _v[2]; _v[0] = (nx) ? voffAn[h][0] : voffA[h][0]; _v[1] = (nx) ? voffAn[h][1] : voffA[h][1]; PG8_STAGE(bufoff, gbase, _v); } \
;         else PG8_STAGE(bufoff, (gbase) + (h) * hstepA, voffA[0]); } while (0)
; #define PG8_LDA(dst, b, h) do { _Pragma("unroll") for (int m = 0; m < 4; ++m) _Pragma("unroll") for (int k = 0; k < 2; ++k) dst[m][k] = *(const LAS bf16x8*)(lds + PG8_SA(b, h) + aoff + m * 2048 + k * 1024); } while (0)
; #define PG8_MMA(ai, bj, At, Bt) do { __builtin_amdgcn_s_setprio(1); _Pragma("unroll") for (int m = 0; m < 4; ++m) _Pragma("unroll") for (int n = 0; n < 2; ++n) _Pragma("unroll") for (int k = 0; k < 2; ++k) \
;         acc[ai][bj][m][n] = __builtin_amdgcn_mfma_f32_16x16x32_bf16(Bt[n][k], At[m][k], acc[ai][bj][m][n], 0, 0, 0); __builtin_amdgcn_s_setprio(0); } while (0)
; #define PG8_WAIT_V(n) asm volatile("s_waitcnt vmcnt(" #n ")" ::: "memory")
; #define PG8_WAIT_L(n) asm volatile("s_waitcnt lgkmcnt(" #n ")" ::: "memory")
; #define PG8_BAR __builtin_amdgcn_s_barrier()
; #define PG8_SCHED __builtin_amdgcn_sched_barrier(0)
; template <class Epi, class Sched, bool GATHER, bool ALIGN_EPI>
; __device__ __forceinline__ void gemm_phase(LAS unsigned char* lds, const int wave_, const int K, const int lda, const int ldb, const Sched& S, const Epi& E) {
;     ...
;             PG8_LDA(At, 1, 1); PG8_STAGE(PG8_SB(1, 0), b3, voffB); PG8_STAGE(PG8_SB(1, 1), b3 + hstepB, voffB); PG8_STAGE_A(PG8_SA(1, 0), a3, 0, last);
;             PG8_WAIT_V(8); PG8_WAIT_L(0); PG8_BAR; PG8_MMA(1, 0, At, B0); PG8_MMA(1, 1, At, B1); PG8_BAR; PG8_SCHED;
;         }
	s_setprio 1
	s_waitcnt lgkmcnt(0)
	v_mfma_f32_16x16x32_bf16 v[60:63], v[128:131], v[180:183], v[60:63]
	v_mfma_f32_16x16x32_bf16 v[56:59], v[136:139], v[180:183], v[56:59]
	v_mfma_f32_16x16x32_bf16 v[44:47], v[128:131], v[204:207], v[44:47]
	v_mfma_f32_16x16x32_bf16 v[40:43], v[136:139], v[204:207], v[40:43]
	v_mfma_f32_16x16x32_bf16 v[28:31], v[128:131], v[220:223], v[28:31]
	v_mfma_f32_16x16x32_bf16 v[24:27], v[136:139], v[220:223], v[24:27]
	v_mfma_f32_16x16x32_bf16 v[12:15], v[128:131], v[228:231], v[12:15]
	v_mfma_f32_16x16x32_bf16 v[8:11], v[136:139], v[228:231], v[8:11]
	v_mfma_f32_16x16x32_bf16 v[60:63], v[132:135], v[184:187], v[60:63]
	v_mfma_f32_16x16x32_bf16 v[56:59], v[140:143], v[184:187], v[56:59]
	v_mfma_f32_16x16x32_bf16 v[44:47], v[132:135], v[216:219], v[44:47]
	v_mfma_f32_16x16x32_bf16 v[40:43], v[140:143], v[216:219], v[40:43]
	v_mfma_f32_16x16x32_bf16 v[28:31], v[132:135], v[224:227], v[28:31]
	v_mfma_f32_16x16x32_bf16 v[24:27], v[140:143], v[224:227], v[24:27]
	v_mfma_f32_16x16x32_bf16 v[12:15], v[132:135], v[232:235], v[12:15]
	v_mfma_f32_16x16x32_bf16 v[8:11], v[140:143], v[232:235], v[8:11]
	s_setprio 0
	s_setprio 1
	v_mfma_f32_16x16x32_bf16 v[52:55], v[144:147], v[180:183], v[52:55]
	v_mfma_f32_16x16x32_bf16 v[48:51], v[152:155], v[180:183], v[48:51]
	v_mfma_f32_16x16x32_bf16 v[36:39], v[144:147], v[204:207], v[36:39]
	v_mfma_f32_16x16x32_bf16 v[32:35], v[152:155], v[204:207], v[32:35]
	v_mfma_f32_16x16x32_bf16 v[20:23], v[144:147], v[220:223], v[20:23]
	v_mfma_f32_16x16x32_bf16 v[16:19], v[152:155], v[220:223], v[16:19]
	v_mfma_f32_16x16x32_bf16 v[4:7], v[144:147], v[228:231], v[4:7]
	v_mfma_f32_16x16x32_bf16 v[0:3], v[152:155], v[228:231], v[0:3]
	v_mfma_f32_16x16x32_bf16 v[52:55], v[148:151], v[184:187], v[52:55]
	v_mfma_f32_16x16x32_bf16 v[48:51], v[176:179], v[184:187], v[48:51]
	v_mfma_f32_16x16x32_bf16 v[36:39], v[148:151], v[216:219], v[36:39]
	v_mfma_f32_16x16x32_bf16 v[32:35], v[176:179], v[216:219], v[32:35]
	v_mfma_f32_16x16x32_bf16 v[20:23], v[148:151], v[224:227], v[20:23]
	v_mfma_f32_16x16x32_bf16 v[16:19], v[176:179], v[224:227], v[16:19]
	v_mfma_f32_16x16x32_bf16 v[4:7], v[148:151], v[232:235], v[4:7]
	v_mfma_f32_16x16x32_bf16 v[0:3], v[176:179], v[232:235], v[0:3]
	s_setprio 0
	s_barrier
	s_add_i32 s31, s31, 2
	s_add_u32 s4, s4, 0x100
	s_addc_u32 s5, s5, 0
	s_add_u32 s11, s11, 0x100
	s_addc_u32 s13, s13, 0
	s_cmp_gt_u32 s31, 13
	s_cbranch_scc0 .LBB0_720
	v_readlane_b32 s2, v253, 1
	v_readlane_b32 s3, v253, 2
	s_and_b64 vcc, exec, s[2:3]
	s_cbranch_vccz .LBB0_723
	s_barrier
; template <int M> __device__ __forceinline__ float swz_xor(float v) { return __int_as_float(__builtin_amdgcn_ds_swizzle(__float_as_int(v), (M << 10) | 0x1f)); }
; __device__ __forceinline__ float half_sum(float v) { auto rr = __builtin_amdgcn_permlane32_swap(__float_as_uint(v), __float_as_uint(v), false, false); return __uint_as_float(rr[0]) + __uint_as_float(rr[1]); }
; __device__ __forceinline__ void row_rscale8(const float* part, const int (&rows)[2][4], int fq, float (&rs)[2][4]) {
;     ...
;         for (int m = 0; m < 4; ++m) v[ai][m] = *(const f32x4*)(part + (size_t)rows[ai][m] * 16 + fq * 4);
; #pragma unroll
;     for (int ai = 0; ai < 2; ++ai)
; #pragma unroll
;         for (int m = 0; m < 4; ++m) { float s = (v[ai][m][0] + v[ai][m][1]) + (v[ai][m][2] + v[ai][m][3]); s += swz_xor<16>(s); s = half_sum(s); rs[ai][m] = __builtin_amdgcn_rcpf(sqrtf(s * (1.0f / DM) + EPS)); }
;     __device__ __forceinline__ bool operator()(f32x4 (&acc)[2][2][4][2], const pg8::Unit& u, int wr, int wc, int fr, int fq) const {
;         const int pn = u.pn, row0 = u.pm * 256 + wr * 64 + fr;
;         float rs_[2][4]; { int rows_[2][4];
; #pragma unroll
;             for (int ai = 0; ai < 2; ++ai)
; #pragma unroll
;                 for (int m = 0; m < 4; ++m) rows_[ai][m] = row0 + ai * 128 + m * 16;
;             row_rscale8(part, rows_, fq, rs_); }
.LBB0_723:
	v_lshl_add_u32 v184, s30, 8, v199
	v_ashrrev_i32_e32 v185, 31, v184
	v_or_b32_e32 v196, 16, v184
	v_ashrrev_i32_e32 v197, 31, v196
	v_or_b32_e32 v188, 32, v184
	v_ashrrev_i32_e32 v189, 31, v188
	v_or_b32_e32 v186, 48, v184
	v_ashrrev_i32_e32 v187, 31, v186
	v_add_u32_e32 v182, 0x80, v184
	v_ashrrev_i32_e32 v183, 31, v182
	v_add_u32_e32 v180, 0x90, v184
	v_ashrrev_i32_e32 v181, 31, v180
	v_add_u32_e32 v178, 0xa0, v184
	v_ashrrev_i32_e32 v179, 31, v178
	s_mov_b32 s2, 0xf800000
	v_add_u32_e32 v176, 0xb0, v184
	v_ashrrev_i32_e32 v177, 31, v176
	s_cmp_gt_i32 s29, 7
	v_mov_b64_e32 v[230:231], v[210:211]
	s_nop 1
	v_fmamk_f32 v160, v236, 0x3a800000, v212
	v_cmp_gt_f32_e32 vcc, s2, v160
	v_mul_f32_e32 v190, 0x4f800000, v160
	s_nop 0
	v_cndmask_b32_e32 v160, v160, v190, vcc
	v_sqrt_f32_e32 v190, v160
	s_nop 0
	v_add_u32_e32 v191, -1, v190
	v_fma_f32 v192, -v191, v190, v160
	v_cmp_ge_f32_e64 s[4:5], 0, v192
	v_add_u32_e32 v192, 1, v190
	s_nop 0
	v_cndmask_b32_e64 v191, v190, v191, s[4:5]
	v_fma_f32 v190, -v192, v190, v160
	v_cmp_lt_f32_e64 s[4:5], 0, v190
	s_nop 0
	s_nop 0
	v_cndmask_b32_e64 v190, v191, v192, s[4:5]
	v_mul_f32_e32 v191, 0x37800000, v190
	v_cndmask_b32_e32 v190, v190, v191, vcc
	v_cmp_class_f32_e32 vcc, v160, v248
	v_fmamk_f32 v152, v237, 0x3a800000, v212
	v_mul_f32_e32 v153, 0x4f800000, v152
	v_cndmask_b32_e32 v160, v190, v160, vcc
	v_cmp_gt_f32_e32 vcc, s2, v152
	s_nop 1
	v_cndmask_b32_e32 v152, v152, v153, vcc
	v_sqrt_f32_e32 v153, v152
	s_nop 0
	v_add_u32_e32 v154, -1, v153
	v_fma_f32 v155, -v154, v153, v152
	v_cmp_ge_f32_e64 s[4:5], 0, v155
	v_add_u32_e32 v155, 1, v153
	s_nop 0
	v_cndmask_b32_e64 v154, v153, v154, s[4:5]
	v_fma_f32 v153, -v155, v153, v152
	v_cmp_lt_f32_e64 s[4:5], 0, v153
	s_nop 0
	s_nop 0
	v_cndmask_b32_e64 v153, v154, v155, s[4:5]
	v_mul_f32_e32 v154, 0x37800000, v153
	v_cndmask_b32_e32 v153, v153, v154, vcc
	v_cmp_class_f32_e32 vcc, v152, v248
	v_fmamk_f32 v148, v238, 0x3a800000, v212
	v_mul_f32_e32 v149, 0x4f800000, v148
	v_cndmask_b32_e32 v152, v153, v152, vcc
	v_cmp_gt_f32_e32 vcc, s2, v148
	s_nop 1
	v_cndmask_b32_e32 v148, v148, v149, vcc
	v_sqrt_f32_e32 v149, v148
	s_nop 0
	v_add_u32_e32 v150, -1, v149
	v_fma_f32 v151, -v150, v149, v148
	v_cmp_ge_f32_e64 s[4:5], 0, v151
	v_add_u32_e32 v151, 1, v149
	s_nop 0
	v_cndmask_b32_e64 v150, v149, v150, s[4:5]
	v_fma_f32 v149, -v151, v149, v148
	v_cmp_lt_f32_e64 s[4:5], 0, v149
	s_nop 0
	s_nop 0
	v_cndmask_b32_e64 v149, v150, v151, s[4:5]
	v_mul_f32_e32 v150, 0x37800000, v149
	v_cndmask_b32_e32 v149, v149, v150, vcc
	v_cmp_class_f32_e32 vcc, v148, v248
	v_fmamk_f32 v144, v239, 0x3a800000, v212
	v_mul_f32_e32 v145, 0x4f800000, v144
	v_cndmask_b32_e32 v148, v149, v148, vcc
	v_cmp_gt_f32_e32 vcc, s2, v144
	s_nop 1
	v_cndmask_b32_e32 v144, v144, v145, vcc
	v_sqrt_f32_e32 v145, v144
	s_nop 0
	v_add_u32_e32 v146, -1, v145
	v_fma_f32 v147, -v146, v145, v144
	v_cmp_ge_f32_e64 s[4:5], 0, v147
	v_add_u32_e32 v147, 1, v145
	s_nop 0
	v_cndmask_b32_e64 v146, v145, v146, s[4:5]
	v_fma_f32 v145, -v147, v145, v144
	v_cmp_lt_f32_e64 s[4:5], 0, v145
	s_nop 0
	s_nop 0
	v_cndmask_b32_e64 v145, v146, v147, s[4:5]
	v_mul_f32_e32 v146, 0x37800000, v145
	v_cndmask_b32_e32 v145, v145, v146, vcc
	v_cmp_class_f32_e32 vcc, v144, v248
	v_fmamk_f32 v140, v240, 0x3a800000, v212
	v_mul_f32_e32 v141, 0x4f800000, v140
	v_cndmask_b32_e32 v144, v145, v144, vcc
	v_cmp_gt_f32_e32 vcc, s2, v140
	s_nop 1
	v_cndmask_b32_e32 v140, v140, v141, vcc
	v_sqrt_f32_e32 v141, v140
	s_nop 0
	v_add_u32_e32 v142, -1, v141
	v_fma_f32 v143, -v142, v141, v140
	v_cmp_ge_f32_e64 s[4:5], 0, v143
	v_add_u32_e32 v143, 1, v141
	s_nop 0
	v_cndmask_b32_e64 v142, v141, v142, s[4:5]
	v_fma_f32 v141, -v143, v141, v140
	v_cmp_lt_f32_e64 s[4:5], 0, v141
	s_nop 0
	s_nop 0
	v_cndmask_b32_e64 v141, v142, v143, s[4:5]
	v_mul_f32_e32 v142, 0x37800000, v141
	v_cndmask_b32_e32 v141, v141, v142, vcc
	v_cmp_class_f32_e32 vcc, v140, v248
	v_fmamk_f32 v136, v241, 0x3a800000, v212
	v_mul_f32_e32 v137, 0x4f800000, v136
	v_cndmask_b32_e32 v140, v141, v140, vcc
	v_cmp_gt_f32_e32 vcc, s2, v136
	s_nop 1
	v_cndmask_b32_e32 v136, v136, v137, vcc
	v_sqrt_f32_e32 v137, v136
	s_nop 0
	v_add_u32_e32 v138, -1, v137
	v_fma_f32 v139, -v138, v137, v136
	v_cmp_ge_f32_e64 s[4:5], 0, v139
	v_add_u32_e32 v139, 1, v137
	s_nop 0
	v_cndmask_b32_e64 v138, v137, v138, s[4:5]
	v_fma_f32 v137, -v139, v137, v136
	v_cmp_lt_f32_e64 s[4:5], 0, v137
	s_nop 0
	s_nop 0
	v_cndmask_b32_e64 v137, v138, v139, s[4:5]
	v_mul_f32_e32 v138, 0x37800000, v137
	v_cndmask_b32_e32 v137, v137, v138, vcc
	v_cmp_class_f32_e32 vcc, v136, v248
	v_fmamk_f32 v132, v242, 0x3a800000, v212
	v_mul_f32_e32 v133, 0x4f800000, v132
	v_cndmask_b32_e32 v136, v137, v136, vcc
	v_cmp_gt_f32_e32 vcc, s2, v132
	s_nop 1
	v_cndmask_b32_e32 v132, v132, v133, vcc
	v_sqrt_f32_e32 v133, v132
	v_rcp_f32_e32 v198, v160
	v_rcp_f32_e32 v154, v152
	v_add_u32_e32 v134, -1, v133
	v_fma_f32 v135, -v134, v133, v132
	v_cmp_ge_f32_e64 s[4:5], 0, v135
	v_add_u32_e32 v135, 1, v133
	s_nop 0
	v_cndmask_b32_e64 v134, v133, v134, s[4:5]
	v_fma_f32 v133, -v135, v133, v132
	v_cmp_lt_f32_e64 s[4:5], 0, v133
	s_nop 0
	s_nop 0
	v_cndmask_b32_e64 v133, v134, v135, s[4:5]
	v_mul_f32_e32 v134, 0x37800000, v133
	v_cndmask_b32_e32 v133, v133, v134, vcc
	v_cmp_class_f32_e32 vcc, v132, v248
	v_fmamk_f32 v128, v243, 0x3a800000, v212
	v_mul_f32_e32 v129, 0x4f800000, v128
	v_cndmask_b32_e32 v132, v133, v132, vcc
	v_cmp_gt_f32_e32 vcc, s2, v128
	v_rcp_f32_e32 v202, v148
	v_rcp_f32_e32 v200, v144
	v_cndmask_b32_e32 v128, v128, v129, vcc
	v_sqrt_f32_e32 v129, v128
	v_rcp_f32_e32 v152, v140
	v_rcp_f32_e32 v150, v136
	v_rcp_f32_e32 v148, v132
	v_add_u32_e32 v130, -1, v129
	v_fma_f32 v131, -v130, v129, v128
	v_cmp_ge_f32_e64 s[4:5], 0, v131
	v_add_u32_e32 v131, 1, v129
	s_nop 0
	v_cndmask_b32_e64 v130, v129, v130, s[4:5]
	v_fma_f32 v129, -v131, v129, v128
	v_cmp_lt_f32_e64 s[4:5], 0, v129
	s_nop 1
	v_cndmask_b32_e64 v129, v130, v131, s[4:5]
	v_mul_f32_e32 v130, 0x37800000, v129
	v_cndmask_b32_e32 v129, v129, v130, vcc
	v_cmp_class_f32_e32 vcc, v128, v248
	s_mov_b64 s[4:5], -1
	s_nop 0
	v_cndmask_b32_e32 v128, v129, v128, vcc
	v_rcp_f32_e32 v146, v128
	s_cbranch_scc1 .LBB0_726
	s_andn2_b64 vcc, exec, s[4:5]
	s_cbranch_vccz .LBB0_735

.LBB0_825:
	ds_read_b64_tr_b16 v[190:191], v234 offset:0x600
	ds_read_b64_tr_b16 v[192:193], v234 offset:0xe00
	ds_read_b64_tr_b16 v[236:237], v234 offset:0x1600
	ds_read_b64_tr_b16 v[238:239], v234 offset:0x1e00
	ds_read_b64_tr_b16 v[240:241], v234 offset:0x2600
	ds_read_b64_tr_b16 v[242:243], v234 offset:0x2e00
	ds_read_b64_tr_b16 v[244:245], v234 offset:0x3600
	ds_read_b64_tr_b16 v[246:247], v234 offset:0x3e00
	s_waitcnt lgkmcnt(8)
	v_mfma_f32_32x32x16_bf16 v[32:47], v[96:99], v[124:127], v[32:47]
	v_exp_f32_e32 v128, v128
	v_exp_f32_e32 v129, v129
	v_exp_f32_e32 v130, v130
	v_mfma_f32_32x32x16_bf16 v[32:47], v[120:123], v[116:119], v[32:47]
	v_exp_f32_e32 v131, v131
	v_exp_f32_e32 v132, v132
	v_exp_f32_e32 v133, v133
	v_mfma_f32_32x32x16_bf16 v[32:47], v[104:107], v[112:115], v[32:47]
	v_exp_f32_e32 v134, v134
	v_exp_f32_e32 v135, v135
	v_exp_f32_e32 v136, v136
	v_mfma_f32_32x32x16_bf16 v[32:47], v[100:103], v[108:111], v[32:47]
	v_exp_f32_e32 v137, v137
	v_exp_f32_e32 v138, v138
	v_exp_f32_e32 v139, v139
	s_waitcnt lgkmcnt(0)
	s_lshl_b32 s2, s41, 14
	s_add_i32 s2, s2, 0
	v_add_u32_e32 v64, s2, v218
	s_lshl_b32 s3, s41, 13
	s_waitcnt vmcnt(2)
	ds_write_b128 v64, v[178:181]
	v_add_u32_e32 v64, s2, v219
	s_sub_i32 s2, s2, s3
	s_waitcnt vmcnt(1)
	ds_write_b128 v64, v[182:185]
	v_add_u32_e32 v64, s2, v220
	s_waitcnt vmcnt(0)
	ds_write_b128 v64, v[186:189] offset:49152
	v_mfma_f32_32x32x16_bf16 v[16:31], v[96:99], v[190:193], v[16:31]
	v_exp_f32_e32 v140, v140
	v_exp_f32_e32 v141, v141
	v_exp_f32_e32 v142, v142
	v_mfma_f32_32x32x16_bf16 v[16:31], v[120:123], v[236:239], v[16:31]
	v_exp_f32_e32 v143, v143
	v_exp_f32_e32 v144, v144
	v_exp_f32_e32 v145, v145
	v_cmp_gt_f32_e32 vcc, 1.0, v233
	v_mfma_f32_32x32x16_bf16 v[16:31], v[104:107], v[240:243], v[16:31]
	v_exp_f32_e32 v146, v146
	v_exp_f32_e32 v147, v147
	v_exp_f32_e32 v148, v148
	v_mfma_f32_32x32x16_bf16 v[16:31], v[100:103], v[244:247], v[16:31]
	v_exp_f32_e32 v149, v149
	v_exp_f32_e32 v150, v150
	v_exp_f32_e32 v151, v151
	s_cbranch_vccz .LBB0_829
	s_and_saveexec_b64 s[12:13], s[0:1]
	ds_write_b32 v214, v233 offset:128
	s_or_b64 exec, exec, s[12:13]
	s_waitcnt lgkmcnt(0)
	v_add_u32_e32 v108, v213, v160
	ds_read_b128 v[96:99], v108 offset:224
	ds_read_b128 v[100:103], v108 offset:192
	ds_read_b128 v[104:107], v108 offset:160
	ds_read_b128 v[108:111], v108 offset:128
	s_waitcnt lgkmcnt(3)
	v_pk_mul_f32 v[12:13], v[12:13], v[96:97]
	s_waitcnt lgkmcnt(2)
	v_pk_mul_f32 v[8:9], v[8:9], v[100:101]
	s_waitcnt lgkmcnt(1)
	v_pk_mul_f32 v[4:5], v[4:5], v[104:105]
	v_pk_mul_f32 v[14:15], v[14:15], v[98:99]
	v_pk_mul_f32 v[10:11], v[10:11], v[102:103]
	v_pk_mul_f32 v[6:7], v[6:7], v[106:107]
	s_waitcnt lgkmcnt(0)
	v_pk_mul_f32 v[2:3], v[2:3], v[110:111]
	v_pk_mul_f32 v[0:1], v[0:1], v[108:109]
	v_pk_mul_f32 v[60:61], v[60:61], v[96:97]
	v_pk_mul_f32 v[56:57], v[56:57], v[100:101]
	v_pk_mul_f32 v[52:53], v[52:53], v[104:105]
	v_pk_mul_f32 v[62:63], v[62:63], v[98:99]
	v_pk_mul_f32 v[58:59], v[58:59], v[102:103]
	v_pk_mul_f32 v[54:55], v[54:55], v[106:107]
	v_pk_mul_f32 v[50:51], v[50:51], v[110:111]
	v_pk_mul_f32 v[48:49], v[48:49], v[108:109]
	v_pk_mul_f32 v[44:45], v[44:45], v[96:97]
	v_pk_mul_f32 v[40:41], v[40:41], v[100:101]
	v_pk_mul_f32 v[36:37], v[36:37], v[104:105]
	v_pk_mul_f32 v[46:47], v[46:47], v[98:99]
	v_pk_mul_f32 v[42:43], v[42:43], v[102:103]
	v_pk_mul_f32 v[38:39], v[38:39], v[106:107]
	v_pk_mul_f32 v[34:35], v[34:35], v[110:111]
	v_pk_mul_f32 v[32:33], v[32:33], v[108:109]
	v_pk_mul_f32 v[28:29], v[28:29], v[96:97]
	v_pk_mul_f32 v[24:25], v[24:25], v[100:101]
	v_pk_mul_f32 v[20:21], v[20:21], v[104:105]
	v_pk_mul_f32 v[30:31], v[30:31], v[98:99]
	v_pk_mul_f32 v[26:27], v[26:27], v[102:103]
	v_pk_mul_f32 v[22:23], v[22:23], v[106:107]
	v_pk_mul_f32 v[18:19], v[18:19], v[110:111]
	v_pk_mul_f32 v[16:17], v[16:17], v[108:109]

.LBB0_830:
	ds_read_b64_tr_b16 v[190:191], v205 offset:0x600
	ds_read_b64_tr_b16 v[192:193], v205 offset:0xe00
	ds_read_b64_tr_b16 v[234:235], v205 offset:0x1600
	ds_read_b64_tr_b16 v[236:237], v205 offset:0x1e00
	ds_read_b64_tr_b16 v[238:239], v205 offset:0x2600
	ds_read_b64_tr_b16 v[240:241], v205 offset:0x2e00
	ds_read_b64_tr_b16 v[242:243], v205 offset:0x3600
	ds_read_b64_tr_b16 v[244:245], v205 offset:0x3e00
	s_add_i32 s2, s41, 1
	s_waitcnt lgkmcnt(8)
	s_cmp_lg_u32 s41, 2
	s_cselect_b32 s42, s2, 0
	v_mfma_f32_32x32x16_bf16 v[32:47], v[152:155], v[156:159], v[32:47]
	v_exp_f32_e32 v96, v96
	v_exp_f32_e32 v97, v97
	v_exp_f32_e32 v98, v98
	v_mfma_f32_32x32x16_bf16 v[32:47], v[136:139], v[148:151], v[32:47]
	v_exp_f32_e32 v99, v99
	v_exp_f32_e32 v100, v100
	v_exp_f32_e32 v101, v101
	v_mfma_f32_32x32x16_bf16 v[32:47], v[132:135], v[144:147], v[32:47]
	v_exp_f32_e32 v102, v102
	v_exp_f32_e32 v103, v103
	v_exp_f32_e32 v104, v104
	v_mfma_f32_32x32x16_bf16 v[32:47], v[128:131], v[140:143], v[32:47]
	v_exp_f32_e32 v105, v105
	v_exp_f32_e32 v106, v106
	v_exp_f32_e32 v107, v107
	s_waitcnt lgkmcnt(0)
	s_lshl_b32 s2, s42, 14
	s_add_i32 s2, s2, 0
	v_add_u32_e32 v64, s2, v218
	s_waitcnt vmcnt(2)
	ds_write_b128 v64, v[178:181]
	v_add_u32_e32 v64, s2, v219
	s_waitcnt vmcnt(1)
	ds_write_b128 v64, v[182:185]
	v_lshl_add_u32 v64, s42, 13, v221
	s_waitcnt vmcnt(0)
	ds_write_b128 v64, v[186:189] offset:49152
	v_mfma_f32_32x32x16_bf16 v[16:31], v[152:155], v[190:193], v[16:31]
	v_exp_f32_e32 v108, v108
	v_exp_f32_e32 v109, v109
	v_exp_f32_e32 v110, v110
	v_mfma_f32_32x32x16_bf16 v[16:31], v[136:139], v[234:237], v[16:31]
	v_exp_f32_e32 v111, v111
	v_exp_f32_e32 v112, v112
	v_exp_f32_e32 v113, v113
	v_cmp_gt_f32_e32 vcc, 1.0, v202
	v_mfma_f32_32x32x16_bf16 v[16:31], v[132:135], v[238:241], v[16:31]
	v_exp_f32_e32 v114, v114
	v_exp_f32_e32 v115, v115
	v_exp_f32_e32 v116, v116
	v_mfma_f32_32x32x16_bf16 v[16:31], v[128:131], v[242:245], v[16:31]
	v_exp_f32_e32 v117, v117
	v_exp_f32_e32 v118, v118
	v_exp_f32_e32 v119, v119
	s_cbranch_vccz .LBB0_834
	s_and_saveexec_b64 s[12:13], s[0:1]
	ds_write_b32 v214, v202 offset:128
	s_or_b64 exec, exec, s[12:13]
	s_waitcnt lgkmcnt(0)
	v_add_u32_e32 v140, v213, v160
	ds_read_b128 v[128:131], v140 offset:224
	ds_read_b128 v[132:135], v140 offset:192
	ds_read_b128 v[136:139], v140 offset:160
	ds_read_b128 v[140:143], v140 offset:128
	s_waitcnt lgkmcnt(3)
	v_pk_mul_f32 v[12:13], v[12:13], v[128:129]
	s_waitcnt lgkmcnt(2)
	v_pk_mul_f32 v[8:9], v[8:9], v[132:133]
	s_waitcnt lgkmcnt(1)
	v_pk_mul_f32 v[4:5], v[4:5], v[136:137]
	v_pk_mul_f32 v[14:15], v[14:15], v[130:131]
	v_pk_mul_f32 v[10:11], v[10:11], v[134:135]
	v_pk_mul_f32 v[6:7], v[6:7], v[138:139]
	s_waitcnt lgkmcnt(0)
	v_pk_mul_f32 v[2:3], v[2:3], v[142:143]
	v_pk_mul_f32 v[0:1], v[0:1], v[140:141]
	v_pk_mul_f32 v[60:61], v[60:61], v[128:129]
	v_pk_mul_f32 v[56:57], v[56:57], v[132:133]
	v_pk_mul_f32 v[52:53], v[52:53], v[136:137]
	v_pk_mul_f32 v[62:63], v[62:63], v[130:131]
	v_pk_mul_f32 v[58:59], v[58:59], v[134:135]
	v_pk_mul_f32 v[54:55], v[54:55], v[138:139]
	v_pk_mul_f32 v[50:51], v[50:51], v[142:143]
	v_pk_mul_f32 v[48:49], v[48:49], v[140:141]
	v_pk_mul_f32 v[44:45], v[44:45], v[128:129]
	v_pk_mul_f32 v[40:41], v[40:41], v[132:133]
	v_pk_mul_f32 v[36:37], v[36:37], v[136:137]
	v_pk_mul_f32 v[46:47], v[46:47], v[130:131]
	v_pk_mul_f32 v[42:43], v[42:43], v[134:135]
	v_pk_mul_f32 v[38:39], v[38:39], v[138:139]
	v_pk_mul_f32 v[34:35], v[34:35], v[142:143]
	v_pk_mul_f32 v[32:33], v[32:33], v[140:141]
	v_pk_mul_f32 v[28:29], v[28:29], v[128:129]
	v_pk_mul_f32 v[24:25], v[24:25], v[132:133]
	v_pk_mul_f32 v[20:21], v[20:21], v[136:137]
	v_pk_mul_f32 v[30:31], v[30:31], v[130:131]
	v_pk_mul_f32 v[26:27], v[26:27], v[134:135]
	v_pk_mul_f32 v[22:23], v[22:23], v[138:139]
	v_pk_mul_f32 v[18:19], v[18:19], v[142:143]
	v_pk_mul_f32 v[16:17], v[16:17], v[140:141]

.LBB0_839:
	ds_read_b64_tr_b16 v[132:133], v217 offset:0x600
	ds_read_b64_tr_b16 v[134:135], v217 offset:0xe00
	ds_read_b64_tr_b16 v[136:137], v217 offset:0x1600
	ds_read_b64_tr_b16 v[138:139], v217 offset:0x1e00
	ds_read_b64_tr_b16 v[140:141], v217 offset:0x2600
	ds_read_b64_tr_b16 v[142:143], v217 offset:0x2e00
	ds_read_b64_tr_b16 v[144:145], v217 offset:0x3600
	ds_read_b64_tr_b16 v[146:147], v217 offset:0x3e00
	s_waitcnt lgkmcnt(8)
	v_mfma_f32_32x32x16_bf16 v[32:47], v[96:99], v[124:127], v[32:47]
	v_exp_f32_e32 v80, v80
	v_exp_f32_e32 v81, v81
	v_exp_f32_e32 v82, v82
	v_mfma_f32_32x32x16_bf16 v[32:47], v[120:123], v[116:119], v[32:47]
	v_exp_f32_e32 v83, v83
	v_exp_f32_e32 v84, v84
	v_exp_f32_e32 v85, v85
	v_mfma_f32_32x32x16_bf16 v[32:47], v[104:107], v[112:115], v[32:47]
	v_exp_f32_e32 v86, v86
	v_exp_f32_e32 v87, v87
	v_exp_f32_e32 v88, v88
	v_mfma_f32_32x32x16_bf16 v[32:47], v[100:103], v[108:111], v[32:47]
	v_exp_f32_e32 v89, v89
	v_exp_f32_e32 v90, v90
	v_exp_f32_e32 v91, v91
	s_waitcnt lgkmcnt(0)
	v_mfma_f32_32x32x16_bf16 v[16:31], v[96:99], v[132:135], v[16:31]
	v_exp_f32_e32 v92, v92
	v_exp_f32_e32 v93, v93
	v_exp_f32_e32 v94, v94
	v_mfma_f32_32x32x16_bf16 v[16:31], v[120:123], v[136:139], v[16:31]
	v_exp_f32_e32 v95, v95
	v_exp_f32_e32 v64, v64
	v_exp_f32_e32 v65, v65
	v_mfma_f32_32x32x16_bf16 v[16:31], v[104:107], v[140:143], v[16:31]
	v_exp_f32_e32 v66, v66
	v_exp_f32_e32 v67, v67
	v_exp_f32_e32 v68, v68
	v_mfma_f32_32x32x16_bf16 v[16:31], v[100:103], v[144:147], v[16:31]
	v_exp_f32_e32 v69, v69
	v_exp_f32_e32 v70, v70
	v_exp_f32_e32 v71, v71
	v_cmp_gt_f32_e32 vcc, 1.0, v130
	s_cbranch_vccz .LBB0_843
	s_and_saveexec_b64 s[12:13], s[0:1]
	ds_write_b32 v214, v130 offset:128
	s_or_b64 exec, exec, s[12:13]
	s_waitcnt lgkmcnt(0)
	v_add_u32_e32 v108, v213, v160
	ds_read_b128 v[96:99], v108 offset:224
	ds_read_b128 v[100:103], v108 offset:192
	ds_read_b128 v[104:107], v108 offset:160
	ds_read_b128 v[108:111], v108 offset:128
	s_waitcnt lgkmcnt(3)
	v_pk_mul_f32 v[12:13], v[12:13], v[96:97]
	s_waitcnt lgkmcnt(2)
	v_pk_mul_f32 v[8:9], v[8:9], v[100:101]
	s_waitcnt lgkmcnt(1)
	v_pk_mul_f32 v[4:5], v[4:5], v[104:105]
	v_pk_mul_f32 v[14:15], v[14:15], v[98:99]
	v_pk_mul_f32 v[10:11], v[10:11], v[102:103]
	v_pk_mul_f32 v[6:7], v[6:7], v[106:107]
	s_waitcnt lgkmcnt(0)
	v_pk_mul_f32 v[2:3], v[2:3], v[110:111]
	v_pk_mul_f32 v[0:1], v[0:1], v[108:109]
	v_pk_mul_f32 v[60:61], v[60:61], v[96:97]
	v_pk_mul_f32 v[56:57], v[56:57], v[100:101]
	v_pk_mul_f32 v[52:53], v[52:53], v[104:105]
	v_pk_mul_f32 v[62:63], v[62:63], v[98:99]
	v_pk_mul_f32 v[58:59], v[58:59], v[102:103]
	v_pk_mul_f32 v[54:55], v[54:55], v[106:107]
	v_pk_mul_f32 v[50:51], v[50:51], v[110:111]
	v_pk_mul_f32 v[48:49], v[48:49], v[108:109]
	v_pk_mul_f32 v[44:45], v[44:45], v[96:97]
	v_pk_mul_f32 v[40:41], v[40:41], v[100:101]
	v_pk_mul_f32 v[36:37], v[36:37], v[104:105]
	v_pk_mul_f32 v[46:47], v[46:47], v[98:99]
	v_pk_mul_f32 v[42:43], v[42:43], v[102:103]
	v_pk_mul_f32 v[38:39], v[38:39], v[106:107]
	v_pk_mul_f32 v[34:35], v[34:35], v[110:111]
	v_pk_mul_f32 v[32:33], v[32:33], v[108:109]
	v_pk_mul_f32 v[28:29], v[28:29], v[96:97]
	v_pk_mul_f32 v[24:25], v[24:25], v[100:101]
	v_pk_mul_f32 v[20:21], v[20:21], v[104:105]
	v_pk_mul_f32 v[30:31], v[30:31], v[98:99]
	v_pk_mul_f32 v[26:27], v[26:27], v[102:103]
	v_pk_mul_f32 v[22:23], v[22:23], v[106:107]
	v_pk_mul_f32 v[18:19], v[18:19], v[110:111]
	v_pk_mul_f32 v[16:17], v[16:17], v[108:109]

.LBB0_848:
	ds_read_b64_tr_b16 v[190:191], v238 offset:0x600
	ds_read_b64_tr_b16 v[192:193], v238 offset:0xe00
	ds_read_b64_tr_b16 v[208:209], v238 offset:0x1600
	ds_read_b64_tr_b16 v[210:211], v238 offset:0x1e00
	ds_read_b64_tr_b16 v[240:241], v238 offset:0x2600
	ds_read_b64_tr_b16 v[242:243], v238 offset:0x2e00
	ds_read_b64_tr_b16 v[244:245], v238 offset:0x3600
	ds_read_b64_tr_b16 v[246:247], v238 offset:0x3e00
	s_waitcnt lgkmcnt(8)
	v_mfma_f32_32x32x16_bf16 v[32:47], v[96:99], v[124:127], v[32:47]
	v_exp_f32_e32 v128, v128
	v_exp_f32_e32 v129, v129
	v_exp_f32_e32 v130, v130
	v_mfma_f32_32x32x16_bf16 v[32:47], v[120:123], v[116:119], v[32:47]
	v_exp_f32_e32 v131, v131
	v_exp_f32_e32 v132, v132
	v_exp_f32_e32 v133, v133
	v_mfma_f32_32x32x16_bf16 v[32:47], v[104:107], v[112:115], v[32:47]
	v_exp_f32_e32 v134, v134
	v_exp_f32_e32 v135, v135
	v_exp_f32_e32 v136, v136
	v_mfma_f32_32x32x16_bf16 v[32:47], v[100:103], v[108:111], v[32:47]
	v_exp_f32_e32 v137, v137
	v_exp_f32_e32 v138, v138
	v_exp_f32_e32 v139, v139
	s_waitcnt lgkmcnt(0)
	s_lshl_b32 s2, s29, 14
	s_add_i32 s2, s2, 0
	v_add_u32_e32 v64, s2, v222
	s_lshl_b32 s3, s29, 13
	s_waitcnt vmcnt(2)
	ds_write_b128 v64, v[178:181]
	v_add_u32_e32 v64, s2, v223
	s_sub_i32 s2, s2, s3
	s_waitcnt vmcnt(1)
	ds_write_b128 v64, v[182:185]
	v_add_u32_e32 v64, s2, v224
	s_waitcnt vmcnt(0)
	ds_write_b128 v64, v[186:189] offset:49152
	v_mfma_f32_32x32x16_bf16 v[16:31], v[96:99], v[190:193], v[16:31]
	v_exp_f32_e32 v140, v140
	v_exp_f32_e32 v141, v141
	v_exp_f32_e32 v142, v142
	v_mfma_f32_32x32x16_bf16 v[16:31], v[120:123], v[208:211], v[16:31]
	v_exp_f32_e32 v143, v143
	v_exp_f32_e32 v144, v144
	v_exp_f32_e32 v145, v145
	v_cmp_gt_f32_e32 vcc, 1.0, v237
	v_mfma_f32_32x32x16_bf16 v[16:31], v[104:107], v[240:243], v[16:31]
	v_exp_f32_e32 v146, v146
	v_exp_f32_e32 v147, v147
	v_exp_f32_e32 v148, v148
	v_mfma_f32_32x32x16_bf16 v[16:31], v[100:103], v[244:247], v[16:31]
	v_exp_f32_e32 v149, v149
	v_exp_f32_e32 v150, v150
	v_exp_f32_e32 v151, v151
	s_cbranch_vccz .LBB0_852
	s_and_saveexec_b64 s[10:11], s[0:1]
	ds_write_b32 v218, v237 offset:128
	s_or_b64 exec, exec, s[10:11]
	s_waitcnt lgkmcnt(0)
	v_add_u32_e32 v108, v217, v160
	ds_read_b128 v[96:99], v108 offset:224
	ds_read_b128 v[100:103], v108 offset:192
	ds_read_b128 v[104:107], v108 offset:160
	ds_read_b128 v[108:111], v108 offset:128
	s_waitcnt lgkmcnt(3)
	v_pk_mul_f32 v[12:13], v[12:13], v[96:97]
	s_waitcnt lgkmcnt(2)
	v_pk_mul_f32 v[8:9], v[8:9], v[100:101]
	s_waitcnt lgkmcnt(1)
	v_pk_mul_f32 v[4:5], v[4:5], v[104:105]
	v_pk_mul_f32 v[14:15], v[14:15], v[98:99]
	v_pk_mul_f32 v[10:11], v[10:11], v[102:103]
	v_pk_mul_f32 v[6:7], v[6:7], v[106:107]
	s_waitcnt lgkmcnt(0)
	v_pk_mul_f32 v[2:3], v[2:3], v[110:111]
	v_pk_mul_f32 v[0:1], v[0:1], v[108:109]
	v_pk_mul_f32 v[60:61], v[60:61], v[96:97]
	v_pk_mul_f32 v[56:57], v[56:57], v[100:101]
	v_pk_mul_f32 v[52:53], v[52:53], v[104:105]
	v_pk_mul_f32 v[62:63], v[62:63], v[98:99]
	v_pk_mul_f32 v[58:59], v[58:59], v[102:103]
	v_pk_mul_f32 v[54:55], v[54:55], v[106:107]
	v_pk_mul_f32 v[50:51], v[50:51], v[110:111]
	v_pk_mul_f32 v[48:49], v[48:49], v[108:109]
	v_pk_mul_f32 v[44:45], v[44:45], v[96:97]
	v_pk_mul_f32 v[40:41], v[40:41], v[100:101]
	v_pk_mul_f32 v[36:37], v[36:37], v[104:105]
	v_pk_mul_f32 v[46:47], v[46:47], v[98:99]
	v_pk_mul_f32 v[42:43], v[42:43], v[102:103]
	v_pk_mul_f32 v[38:39], v[38:39], v[106:107]
	v_pk_mul_f32 v[34:35], v[34:35], v[110:111]
	v_pk_mul_f32 v[32:33], v[32:33], v[108:109]
	v_pk_mul_f32 v[28:29], v[28:29], v[96:97]
	v_pk_mul_f32 v[24:25], v[24:25], v[100:101]
	v_pk_mul_f32 v[20:21], v[20:21], v[104:105]
	v_pk_mul_f32 v[30:31], v[30:31], v[98:99]
	v_pk_mul_f32 v[26:27], v[26:27], v[102:103]
	v_pk_mul_f32 v[22:23], v[22:23], v[106:107]
	v_pk_mul_f32 v[18:19], v[18:19], v[110:111]
	v_pk_mul_f32 v[16:17], v[16:17], v[108:109]

.LBB0_853:
	ds_read_b64_tr_b16 v[190:191], v205 offset:0x600
	ds_read_b64_tr_b16 v[192:193], v205 offset:0xe00
	ds_read_b64_tr_b16 v[208:209], v205 offset:0x1600
	ds_read_b64_tr_b16 v[210:211], v205 offset:0x1e00
	ds_read_b64_tr_b16 v[238:239], v205 offset:0x2600
	ds_read_b64_tr_b16 v[240:241], v205 offset:0x2e00
	ds_read_b64_tr_b16 v[242:243], v205 offset:0x3600
	ds_read_b64_tr_b16 v[244:245], v205 offset:0x3e00
	s_add_i32 s2, s29, 1
	s_waitcnt lgkmcnt(8)
	s_cmp_lg_u32 s29, 2
	s_cselect_b32 s30, s2, 0
	v_mfma_f32_32x32x16_bf16 v[32:47], v[152:155], v[156:159], v[32:47]
	v_exp_f32_e32 v96, v96
	v_exp_f32_e32 v97, v97
	v_exp_f32_e32 v98, v98
	v_mfma_f32_32x32x16_bf16 v[32:47], v[136:139], v[148:151], v[32:47]
	v_exp_f32_e32 v99, v99
	v_exp_f32_e32 v100, v100
	v_exp_f32_e32 v101, v101
	v_mfma_f32_32x32x16_bf16 v[32:47], v[132:135], v[144:147], v[32:47]
	v_exp_f32_e32 v102, v102
	v_exp_f32_e32 v103, v103
	v_exp_f32_e32 v104, v104
	v_mfma_f32_32x32x16_bf16 v[32:47], v[128:131], v[140:143], v[32:47]
	v_exp_f32_e32 v105, v105
	v_exp_f32_e32 v106, v106
	v_exp_f32_e32 v107, v107
	s_waitcnt lgkmcnt(0)
	s_lshl_b32 s2, s30, 14
	s_add_i32 s2, s2, 0
	v_add_u32_e32 v64, s2, v222
	s_waitcnt vmcnt(2)
	ds_write_b128 v64, v[178:181]
	v_add_u32_e32 v64, s2, v223
	s_waitcnt vmcnt(1)
	ds_write_b128 v64, v[182:185]
	v_lshl_add_u32 v64, s30, 13, v225
	s_waitcnt vmcnt(0)
	ds_write_b128 v64, v[186:189] offset:49152
	v_mfma_f32_32x32x16_bf16 v[16:31], v[152:155], v[190:193], v[16:31]
	v_exp_f32_e32 v108, v108
	v_exp_f32_e32 v109, v109
	v_exp_f32_e32 v110, v110
	v_mfma_f32_32x32x16_bf16 v[16:31], v[136:139], v[208:211], v[16:31]
	v_exp_f32_e32 v111, v111
	v_exp_f32_e32 v112, v112
	v_exp_f32_e32 v113, v113
	v_cmp_gt_f32_e32 vcc, 1.0, v202
	v_mfma_f32_32x32x16_bf16 v[16:31], v[132:135], v[238:241], v[16:31]
	v_exp_f32_e32 v114, v114
	v_exp_f32_e32 v115, v115
	v_exp_f32_e32 v116, v116
	v_mfma_f32_32x32x16_bf16 v[16:31], v[128:131], v[242:245], v[16:31]
	v_exp_f32_e32 v117, v117
	v_exp_f32_e32 v118, v118
	v_exp_f32_e32 v119, v119
	s_cbranch_vccz .LBB0_857
	s_and_saveexec_b64 s[10:11], s[0:1]
	ds_write_b32 v218, v202 offset:128
	s_or_b64 exec, exec, s[10:11]
	s_waitcnt lgkmcnt(0)
	v_add_u32_e32 v140, v217, v160
	ds_read_b128 v[128:131], v140 offset:224
	ds_read_b128 v[132:135], v140 offset:192
	ds_read_b128 v[136:139], v140 offset:160
	ds_read_b128 v[140:143], v140 offset:128
	s_waitcnt lgkmcnt(3)
	v_pk_mul_f32 v[12:13], v[12:13], v[128:129]
	s_waitcnt lgkmcnt(2)
	v_pk_mul_f32 v[8:9], v[8:9], v[132:133]
	s_waitcnt lgkmcnt(1)
	v_pk_mul_f32 v[4:5], v[4:5], v[136:137]
	v_pk_mul_f32 v[14:15], v[14:15], v[130:131]
	v_pk_mul_f32 v[10:11], v[10:11], v[134:135]
	v_pk_mul_f32 v[6:7], v[6:7], v[138:139]
	s_waitcnt lgkmcnt(0)
	v_pk_mul_f32 v[2:3], v[2:3], v[142:143]
	v_pk_mul_f32 v[0:1], v[0:1], v[140:141]
	v_pk_mul_f32 v[60:61], v[60:61], v[128:129]
	v_pk_mul_f32 v[56:57], v[56:57], v[132:133]
	v_pk_mul_f32 v[52:53], v[52:53], v[136:137]
	v_pk_mul_f32 v[62:63], v[62:63], v[130:131]
	v_pk_mul_f32 v[58:59], v[58:59], v[134:135]
	v_pk_mul_f32 v[54:55], v[54:55], v[138:139]
	v_pk_mul_f32 v[50:51], v[50:51], v[142:143]
	v_pk_mul_f32 v[48:49], v[48:49], v[140:141]
	v_pk_mul_f32 v[44:45], v[44:45], v[128:129]
	v_pk_mul_f32 v[40:41], v[40:41], v[132:133]
	v_pk_mul_f32 v[36:37], v[36:37], v[136:137]
	v_pk_mul_f32 v[46:47], v[46:47], v[130:131]
	v_pk_mul_f32 v[42:43], v[42:43], v[134:135]
	v_pk_mul_f32 v[38:39], v[38:39], v[138:139]
	v_pk_mul_f32 v[34:35], v[34:35], v[142:143]
	v_pk_mul_f32 v[32:33], v[32:33], v[140:141]
	v_pk_mul_f32 v[28:29], v[28:29], v[128:129]
	v_pk_mul_f32 v[24:25], v[24:25], v[132:133]
	v_pk_mul_f32 v[20:21], v[20:21], v[136:137]
	v_pk_mul_f32 v[30:31], v[30:31], v[130:131]
	v_pk_mul_f32 v[26:27], v[26:27], v[134:135]
	v_pk_mul_f32 v[22:23], v[22:23], v[138:139]
	v_pk_mul_f32 v[18:19], v[18:19], v[142:143]
	v_pk_mul_f32 v[16:17], v[16:17], v[140:141]

.LBB0_862:
	ds_read_b64_tr_b16 v[132:133], v221 offset:0x600
	ds_read_b64_tr_b16 v[134:135], v221 offset:0xe00
	ds_read_b64_tr_b16 v[136:137], v221 offset:0x1600
	ds_read_b64_tr_b16 v[138:139], v221 offset:0x1e00
	ds_read_b64_tr_b16 v[140:141], v221 offset:0x2600
	ds_read_b64_tr_b16 v[142:143], v221 offset:0x2e00
	ds_read_b64_tr_b16 v[144:145], v221 offset:0x3600
	ds_read_b64_tr_b16 v[146:147], v221 offset:0x3e00
	s_waitcnt lgkmcnt(8)
	v_mfma_f32_32x32x16_bf16 v[32:47], v[96:99], v[124:127], v[32:47]
	v_exp_f32_e32 v80, v80
	v_exp_f32_e32 v81, v81
	v_exp_f32_e32 v82, v82
	v_mfma_f32_32x32x16_bf16 v[32:47], v[120:123], v[116:119], v[32:47]
	v_exp_f32_e32 v83, v83
	v_exp_f32_e32 v84, v84
	v_exp_f32_e32 v85, v85
	v_mfma_f32_32x32x16_bf16 v[32:47], v[104:107], v[112:115], v[32:47]
	v_exp_f32_e32 v86, v86
	v_exp_f32_e32 v87, v87
	v_exp_f32_e32 v88, v88
	v_mfma_f32_32x32x16_bf16 v[32:47], v[100:103], v[108:111], v[32:47]
	v_exp_f32_e32 v89, v89
	v_exp_f32_e32 v90, v90
	v_exp_f32_e32 v91, v91
	s_waitcnt lgkmcnt(0)
	v_mfma_f32_32x32x16_bf16 v[16:31], v[96:99], v[132:135], v[16:31]
	v_exp_f32_e32 v92, v92
	v_exp_f32_e32 v93, v93
	v_exp_f32_e32 v94, v94
	v_mfma_f32_32x32x16_bf16 v[16:31], v[120:123], v[136:139], v[16:31]
	v_exp_f32_e32 v95, v95
	v_exp_f32_e32 v64, v64
	v_exp_f32_e32 v65, v65
	v_mfma_f32_32x32x16_bf16 v[16:31], v[104:107], v[140:143], v[16:31]
	v_exp_f32_e32 v66, v66
	v_exp_f32_e32 v67, v67
	v_exp_f32_e32 v68, v68
	v_mfma_f32_32x32x16_bf16 v[16:31], v[100:103], v[144:147], v[16:31]
	v_exp_f32_e32 v69, v69
	v_exp_f32_e32 v70, v70
	v_exp_f32_e32 v71, v71
	v_cmp_gt_f32_e32 vcc, 1.0, v130
	v_mov_b64_e32 v[230:231], 0xff
	s_cbranch_vccz .LBB0_866
	s_and_saveexec_b64 s[10:11], s[0:1]
	ds_write_b32 v218, v130 offset:128
	s_or_b64 exec, exec, s[10:11]
	s_waitcnt lgkmcnt(0)
	v_add_u32_e32 v108, v217, v160
	ds_read_b128 v[96:99], v108 offset:224
	ds_read_b128 v[100:103], v108 offset:192
	ds_read_b128 v[104:107], v108 offset:160
	ds_read_b128 v[108:111], v108 offset:128
	s_waitcnt lgkmcnt(3)
	v_pk_mul_f32 v[12:13], v[12:13], v[96:97]
	s_waitcnt lgkmcnt(2)
	v_pk_mul_f32 v[8:9], v[8:9], v[100:101]
	s_waitcnt lgkmcnt(1)
	v_pk_mul_f32 v[4:5], v[4:5], v[104:105]
	v_pk_mul_f32 v[14:15], v[14:15], v[98:99]
	v_pk_mul_f32 v[10:11], v[10:11], v[102:103]
	v_pk_mul_f32 v[6:7], v[6:7], v[106:107]
	s_waitcnt lgkmcnt(0)
	v_pk_mul_f32 v[2:3], v[2:3], v[110:111]
	v_pk_mul_f32 v[0:1], v[0:1], v[108:109]
	v_pk_mul_f32 v[60:61], v[60:61], v[96:97]
	v_pk_mul_f32 v[56:57], v[56:57], v[100:101]
	v_pk_mul_f32 v[52:53], v[52:53], v[104:105]
	v_pk_mul_f32 v[62:63], v[62:63], v[98:99]
	v_pk_mul_f32 v[58:59], v[58:59], v[102:103]
	v_pk_mul_f32 v[54:55], v[54:55], v[106:107]
	v_pk_mul_f32 v[50:51], v[50:51], v[110:111]
	v_pk_mul_f32 v[48:49], v[48:49], v[108:109]
	v_pk_mul_f32 v[44:45], v[44:45], v[96:97]
	v_pk_mul_f32 v[40:41], v[40:41], v[100:101]
	v_pk_mul_f32 v[36:37], v[36:37], v[104:105]
	v_pk_mul_f32 v[46:47], v[46:47], v[98:99]
	v_pk_mul_f32 v[42:43], v[42:43], v[102:103]
	v_pk_mul_f32 v[38:39], v[38:39], v[106:107]
	v_pk_mul_f32 v[34:35], v[34:35], v[110:111]
	v_pk_mul_f32 v[32:33], v[32:33], v[108:109]
	v_pk_mul_f32 v[28:29], v[28:29], v[96:97]
	v_pk_mul_f32 v[24:25], v[24:25], v[100:101]
	v_pk_mul_f32 v[20:21], v[20:21], v[104:105]
	v_pk_mul_f32 v[30:31], v[30:31], v[98:99]
	v_pk_mul_f32 v[26:27], v[26:27], v[102:103]
	v_pk_mul_f32 v[22:23], v[22:23], v[106:107]
	v_pk_mul_f32 v[18:19], v[18:19], v[110:111]
	v_pk_mul_f32 v[16:17], v[16:17], v[108:109]

; #define LAS __attribute__((address_space(3)))
; __global__ void __launch_bounds__(512, 2) fwd(Args args) {
;     extern __shared__ __attribute__((aligned(16))) unsigned char lds_raw[];
;     LAS unsigned char* lds = (LAS unsigned char*)lds_raw;
;     const int tid = threadIdx.x, lane = tid & 63, wave = __builtin_amdgcn_readfirstlane(tid >> 6);
	.amdhsa_kernel _Z3fwd4Args
		.amdhsa_group_segment_fixed_size 0
		.amdhsa_private_segment_fixed_size 0
		.amdhsa_kernarg_size 472
		.amdhsa_user_sgpr_count 2
		.amdhsa_user_sgpr_dispatch_ptr 0
		.amdhsa_user_sgpr_queue_ptr 0
		.amdhsa_user_sgpr_kernarg_segment_ptr 1
		.amdhsa_user_sgpr_dispatch_id 0
		.amdhsa_user_sgpr_kernarg_preload_length 0
		.amdhsa_user_sgpr_kernarg_preload_offset 0
		.amdhsa_user_sgpr_private_segment_size 0
		.amdhsa_uses_dynamic_stack 0
		.amdhsa_enable_private_segment 0
		.amdhsa_system_sgpr_workgroup_id_x 1
		.amdhsa_system_sgpr_workgroup_id_y 0
		.amdhsa_system_sgpr_workgroup_id_z 0
		.amdhsa_system_sgpr_workgroup_info 0
		.amdhsa_system_vgpr_workitem_id 0
		.amdhsa_next_free_vgpr 256
		.amdhsa_next_free_sgpr 102
		.amdhsa_accum_offset 256
		.amdhsa_reserve_vcc 1
		.amdhsa_float_round_mode_32 0
		.amdhsa_float_round_mode_16_64 0
		.amdhsa_float_denorm_mode_32 3
		.amdhsa_float_denorm_mode_16_64 3
		.amdhsa_dx10_clamp 1
		.amdhsa_ieee_mode 1
		.amdhsa_fp16_overflow 0
		.amdhsa_tg_split 0
		.amdhsa_exception_fp_ieee_invalid_op 0
		.amdhsa_exception_fp_denorm_src 0
		.amdhsa_exception_fp_ieee_div_zero 0
		.amdhsa_exception_fp_ieee_overflow 0
		.amdhsa_exception_fp_ieee_underflow 0
		.amdhsa_exception_fp_ieee_inexact 0
		.amdhsa_exception_int_div_zero 0
	.end_amdhsa_kernel

; __global__ void __launch_bounds__(512, 2) fwd(Args args) {
amdhsa.kernels:
  - .agpr_count:     0
    .args:
      - .offset:         0
        .size:           216
        .value_kind:     by_value
      - .offset:         216
        .size:           4
        .value_kind:     hidden_block_count_x
      - .offset:         220
        .size:           4
        .value_kind:     hidden_block_count_y
      - .offset:         224
        .size:           4
        .value_kind:     hidden_block_count_z
      - .offset:         228
        .size:           2
        .value_kind:     hidden_group_size_x
      - .offset:         230
        .size:           2
        .value_kind:     hidden_group_size_y
      - .offset:         232
        .size:           2
        .value_kind:     hidden_group_size_z
      - .offset:         234
        .size:           2
        .value_kind:     hidden_remainder_x
      - .offset:         236
        .size:           2
        .value_kind:     hidden_remainder_y
      - .offset:         238
        .size:           2
        .value_kind:     hidden_remainder_z
      - .offset:         256
        .size:           8
        .value_kind:     hidden_global_offset_x
      - .offset:         264
        .size:           8
        .value_kind:     hidden_global_offset_y
      - .offset:         272
        .size:           8
        .value_kind:     hidden_global_offset_z
      - .offset:         280
        .size:           2
        .value_kind:     hidden_grid_dims
      - .offset:         336
        .size:           4
        .value_kind:     hidden_dynamic_lds_size
    .group_segment_fixed_size: 0
    .kernarg_segment_align: 8
    .kernarg_segment_size: 472
    .language:       OpenCL C
    .language_version:
      - 2
      - 0
    .max_flat_workgroup_size: 512
    .name:           _Z3fwd4Args
    .private_segment_fixed_size: 0
    .sgpr_count:     108
    .sgpr_spill_count: 265
    .symbol:         _Z3fwd4Args.kd
    .uniform_work_group_size: 1
    .uses_dynamic_stack: false
    .vgpr_count:     256
    .vgpr_spill_count: 0
    .wavefront_size: 64
